# two-accumulator indexer scoring + float-compare pass 2 + sc1 mask/quant loads replacing 4 acquire invalidates + no wbl2 after write-through-only phases
# speedup vs baseline: 1.0068x; 1.0051x over previous
; __device__ __forceinline__ unsigned xb_add(unsigned* p, unsigned v) { return __hip_atomic_fetch_add(p, v, __ATOMIC_RELAXED, __HIP_MEMORY_SCOPE_AGENT); }
; __device__ __forceinline__ void xcd_barrier_impl(const XcdBarrier& b, bool leader) {
;     ...
;         const unsigned old = xb_add(&bar[XB_XSUB(b.x)], 1u);
;         const unsigned gen = old / nloc;
;         if (old + 1u == (gen + 1u) * nloc) {
;             __builtin_amdgcn_fence(__ATOMIC_RELEASE, "agent");
;             asm volatile("s_waitcnt vmcnt(0)" ::: "memory");
;             const unsigned og = xb_add(&bar[XB_TOP], 1u);
.LBB0_329:
	s_andn2_saveexec_b64 s[0:1], s[8:9]
	s_cbranch_execz .LBB0_346
	s_mov_b64 s[10:11], exec
	s_waitcnt lgkmcnt(0)
	s_waitcnt vmcnt(0)
	v_mbcnt_lo_u32_b32 v2, s10, 0
	s_add_u32 s8, s6, 0x7400
	v_mbcnt_hi_u32_b32 v2, s11, v2
	s_addc_u32 s9, s7, 0
	v_cmp_eq_u32_e32 vcc, 0, v2
	s_and_saveexec_b64 s[12:13], vcc
	s_cbranch_execz .LBB0_332
	s_bcnt1_i32_b64 s0, s[10:11]
	v_mov_b32_e32 v3, s0
	global_atomic_add v3, v1, v3, s[8:9] sc0

; __device__ __forceinline__ unsigned xb_ld(unsigned* p)              { return __hip_atomic_load(p, __ATOMIC_RELAXED, __HIP_MEMORY_SCOPE_AGENT); }
; #define XB_SPIN(cond, bar) do { unsigned _sp = 0; while (cond) { __builtin_amdgcn_s_sleep(1); \
;     if ((++_sp & 255u) == 0u) { if (xb_ld(&(bar)[XB_TMO])) break; if (_sp > XB_SPIN_CAP) { atomicAdd(&(bar)[XB_TMO], 1u); break; } } } } while (0)
; __device__ __forceinline__ void xcd_barrier_impl(const XcdBarrier& b, bool leader) {
;     ...
;             __builtin_amdgcn_fence(__ATOMIC_ACQUIRE, "agent");
;             asm volatile("s_waitcnt vmcnt(0)" ::: "memory");
;         } else {
;             XB_SPIN(xb_ld(&bar[XB_TOP]) < (gen + 1u) * nx, bar);
;             __builtin_amdgcn_fence(__ATOMIC_ACQUIRE, "agent");
;             asm volatile("s_waitcnt vmcnt(0)" ::: "memory");
.LBB0_491:
	s_or_b64 exec, exec, s[12:13]
	s_waitcnt vmcnt(0)
	s_waitcnt vmcnt(0)

; __device__ __forceinline__ unsigned xb_ld(unsigned* p)              { return __hip_atomic_load(p, __ATOMIC_RELAXED, __HIP_MEMORY_SCOPE_AGENT); }
; #define XB_SPIN(cond, bar) do { unsigned _sp = 0; while (cond) { __builtin_amdgcn_s_sleep(1); \
;     if ((++_sp & 255u) == 0u) { if (xb_ld(&(bar)[XB_TMO])) break; if (_sp > XB_SPIN_CAP) { atomicAdd(&(bar)[XB_TMO], 1u); break; } } } } while (0)
; __device__ __forceinline__ void xcd_barrier_impl(const XcdBarrier& b, bool leader) {
;     ...
;             __builtin_amdgcn_fence(__ATOMIC_ACQUIRE, "agent");
;             asm volatile("s_waitcnt vmcnt(0)" ::: "memory");
;         } else {
;             XB_SPIN(xb_ld(&bar[XB_TOP]) < (gen + 1u) * nx, bar);
;             __builtin_amdgcn_fence(__ATOMIC_ACQUIRE, "agent");
;             asm volatile("s_waitcnt vmcnt(0)" ::: "memory");
.LBB0_508:
	s_or_b64 exec, exec, s[10:11]
	s_waitcnt vmcnt(0)
	s_waitcnt vmcnt(0)

; __device__ __forceinline__ float relu_i(float p) { const int i = __float_as_int(p); return __int_as_float(i > 0 ? i : 0); }
; __device__ __forceinline__ void idx_scores_k(f32x16& sc, const bf16x8 (&kf)[4], const bf16x8 (&qf)[16], const f32x4& w) {
;     f32x16 p0 = f32x16{}, p1 = f32x16{};
; #pragma unroll
;     for (int d0 = 0; d0 < 4; ++d0) p0 = __builtin_amdgcn_mfma_f32_32x32x16_bf16(kf[d0], qf[d0], p0, 0, 0, 0);
; #pragma unroll
;     for (int d0 = 0; d0 < 4; ++d0) p1 = __builtin_amdgcn_mfma_f32_32x32x16_bf16(kf[d0], qf[4 + d0], p1, 0, 0, 0);
; #pragma unroll
;     for (int r = 0; r < 16; ++r) sc[r] = w[0] * relu_i(p0[r]);
;     p0 = f32x16{};
; #pragma unroll
;     for (int d0 = 0; d0 < 4; ++d0) p0 = __builtin_amdgcn_mfma_f32_32x32x16_bf16(kf[d0], qf[8 + d0], p0, 0, 0, 0);
; #pragma unroll
;     for (int r = 0; r < 16; ++r) sc[r] = fmaf(w[1], relu_i(p1[r]), sc[r]);
;     p1 = f32x16{};
; #pragma unroll
;     for (int d0 = 0; d0 < 4; ++d0) p1 = __builtin_amdgcn_mfma_f32_32x32x16_bf16(kf[d0], qf[12 + d0], p1, 0, 0, 0);
; #pragma unroll
;     for (int r = 0; r < 16; ++r) sc[r] = fmaf(w[2], relu_i(p0[r]), sc[r]);
; #pragma unroll
;     for (int r = 0; r < 16; ++r) sc[r] = fmaf(w[3], relu_i(p1[r]), sc[r]);
; }
; template <int PASS> __device__ __forceinline__ void idx_pass(const bf16_t* KIb, const bf16x8 (&qf)[16], const f32x4& w, int jd, int tq, int wid, int r32, int hi, unsigned khi, unsigned klo, bool cand, LAS unsigned char* L) {
;     ...
;     for (; j <= jd; j += 8) {
;         const bool diag = (j == jd);
;         idx_loadk(kB, KIb + (size_t)(j * 64 + 32) * 64, r32, hi);
;         f32x16 sc; idx_scores_k(sc, kA, qf, w);
;         unsigned lo, elo, hw, ehw;
;         if (diag) idx_half<PASS, true>(lo, elo, sc, j * 64, tq, r32, hi, khi, klo, cand, L); else idx_half<PASS, false>(lo, elo, sc, j * 64, tq, r32, hi, khi, klo, cand, L);
;         if (j + 8 <= jd) idx_loadk(kA, KIb + (size_t)((j + 8) * 64) * 64, r32, hi);
.LBB0_712:
	s_add_i32 s0, s21, s20
	s_cmp_lg_u32 s0, 8
	s_cselect_b64 s[14:15], -1, 0
	s_add_i32 s0, s10, 0xfffffe20
	s_ashr_i32 s1, s0, 31
	s_lshl_b64 s[0:1], s[0:1], 7
	v_lshl_add_u64 v[2:3], v[50:51], 0, s[0:1]
	global_load_dwordx4 v[46:49], v[2:3], off
	global_load_dwordx4 v[42:45], v[2:3], off offset:32
	global_load_dwordx4 v[38:41], v[2:3], off offset:64
	global_load_dwordx4 v[34:37], v[2:3], off offset:96
	s_and_b64 vcc, exec, s[14:15]
	s_waitcnt vmcnt(7) lgkmcnt(14)
	v_mfma_f32_32x32x16_bf16 v[2:17], v[18:21], v[70:73], 0
	s_waitcnt vmcnt(6)
	v_mfma_f32_32x32x16_bf16 v[2:17], v[22:25], v[74:77], v[2:17]
	s_waitcnt vmcnt(5) lgkmcnt(13)
	v_mfma_f32_32x32x16_bf16 v[2:17], v[26:29], v[78:81], v[2:17]
	s_waitcnt vmcnt(4) lgkmcnt(12)
	v_mfma_f32_32x32x16_bf16 v[2:17], v[30:33], v[82:85], v[2:17]
	s_waitcnt lgkmcnt(11)
	v_mfma_f32_32x32x16_bf16 v[180:195], v[18:21], v[86:89], 0
	s_waitcnt lgkmcnt(10)
	v_mfma_f32_32x32x16_bf16 v[180:195], v[22:25], v[90:93], v[180:195]
	s_waitcnt lgkmcnt(9)
	v_mfma_f32_32x32x16_bf16 v[180:195], v[26:29], v[94:97], v[180:195]
	s_waitcnt lgkmcnt(8)
	v_mfma_f32_32x32x16_bf16 v[180:195], v[30:33], v[98:101], v[180:195]
	s_nop 3
	v_max_i32_e32 v200, 0, v2
	v_mul_f32_e32 v136, v66, v200
	v_max_i32_e32 v200, 0, v3
	v_mul_f32_e32 v135, v66, v200
	v_max_i32_e32 v200, 0, v4
	v_mul_f32_e32 v134, v66, v200
	v_max_i32_e32 v200, 0, v5
	v_mul_f32_e32 v65, v66, v200
	v_max_i32_e32 v200, 0, v6
	v_mul_f32_e32 v64, v66, v200
	v_max_i32_e32 v200, 0, v7
	v_mul_f32_e32 v63, v66, v200
	v_max_i32_e32 v200, 0, v8
	v_mul_f32_e32 v62, v66, v200
	v_max_i32_e32 v200, 0, v9
	v_mul_f32_e32 v61, v66, v200
	v_max_i32_e32 v200, 0, v10
	v_mul_f32_e32 v60, v66, v200
	v_max_i32_e32 v200, 0, v11
	v_mul_f32_e32 v59, v66, v200
	v_max_i32_e32 v200, 0, v12
	v_mul_f32_e32 v58, v66, v200
	v_max_i32_e32 v200, 0, v13
	v_mul_f32_e32 v57, v66, v200
	v_max_i32_e32 v200, 0, v14
	v_mul_f32_e32 v56, v66, v200
	v_max_i32_e32 v200, 0, v15
	v_mul_f32_e32 v55, v66, v200
	v_max_i32_e32 v200, 0, v16
	v_mul_f32_e32 v54, v66, v200
	v_max_i32_e32 v200, 0, v17
	v_mul_f32_e32 v53, v66, v200
	s_waitcnt lgkmcnt(7)
	v_mfma_f32_32x32x16_bf16 v[2:17], v[18:21], v[102:105], 0
	s_waitcnt lgkmcnt(6)
	v_mfma_f32_32x32x16_bf16 v[2:17], v[22:25], v[106:109], v[2:17]
	s_waitcnt lgkmcnt(5)
	v_mfma_f32_32x32x16_bf16 v[2:17], v[26:29], v[110:113], v[2:17]
	s_waitcnt lgkmcnt(4)
	v_mfma_f32_32x32x16_bf16 v[2:17], v[30:33], v[114:117], v[2:17]
	v_max_i32_e32 v200, 0, v180
	v_fmac_f32_e32 v136, v67, v200
	v_max_i32_e32 v200, 0, v181
	v_fmac_f32_e32 v135, v67, v200
	v_max_i32_e32 v200, 0, v182
	v_fmac_f32_e32 v134, v67, v200
	v_max_i32_e32 v200, 0, v183
	v_fmac_f32_e32 v65, v67, v200
	v_max_i32_e32 v200, 0, v184
	v_fmac_f32_e32 v64, v67, v200
	v_max_i32_e32 v200, 0, v185
	v_fmac_f32_e32 v63, v67, v200
	v_max_i32_e32 v200, 0, v186
	v_fmac_f32_e32 v62, v67, v200
	v_max_i32_e32 v200, 0, v187
	v_fmac_f32_e32 v61, v67, v200
	v_max_i32_e32 v200, 0, v188
	v_fmac_f32_e32 v60, v67, v200
	v_max_i32_e32 v200, 0, v189
	v_fmac_f32_e32 v59, v67, v200
	v_max_i32_e32 v200, 0, v190
	v_fmac_f32_e32 v58, v67, v200
	v_max_i32_e32 v200, 0, v191
	v_fmac_f32_e32 v57, v67, v200
	v_max_i32_e32 v200, 0, v192
	v_fmac_f32_e32 v56, v67, v200
	v_max_i32_e32 v200, 0, v193
	v_fmac_f32_e32 v55, v67, v200
	v_max_i32_e32 v200, 0, v194
	v_fmac_f32_e32 v54, v67, v200
	v_max_i32_e32 v200, 0, v195
	v_fmac_f32_e32 v53, v67, v200
	s_waitcnt lgkmcnt(3)
	v_mfma_f32_32x32x16_bf16 v[180:195], v[18:21], v[118:121], 0
	s_waitcnt lgkmcnt(2)
	v_mfma_f32_32x32x16_bf16 v[180:195], v[22:25], v[122:125], v[180:195]
	s_waitcnt lgkmcnt(1)
	v_mfma_f32_32x32x16_bf16 v[180:195], v[26:29], v[126:129], v[180:195]
	s_waitcnt lgkmcnt(0)
	v_mfma_f32_32x32x16_bf16 v[180:195], v[30:33], v[130:133], v[180:195]
	v_max_i32_e32 v200, 0, v2
	v_fmac_f32_e32 v136, v68, v200
	v_max_i32_e32 v200, 0, v3
	v_fmac_f32_e32 v135, v68, v200
	v_max_i32_e32 v200, 0, v4
	v_fmac_f32_e32 v134, v68, v200
	v_max_i32_e32 v200, 0, v5
	v_fmac_f32_e32 v65, v68, v200
	v_max_i32_e32 v200, 0, v6
	v_fmac_f32_e32 v64, v68, v200
	v_max_i32_e32 v200, 0, v7
	v_fmac_f32_e32 v63, v68, v200
	v_max_i32_e32 v200, 0, v8
	v_fmac_f32_e32 v62, v68, v200
	v_max_i32_e32 v200, 0, v9
	v_fmac_f32_e32 v61, v68, v200
	v_max_i32_e32 v200, 0, v10
	v_fmac_f32_e32 v60, v68, v200
	v_max_i32_e32 v200, 0, v11
	v_fmac_f32_e32 v59, v68, v200
	v_max_i32_e32 v200, 0, v12
	v_fmac_f32_e32 v58, v68, v200
	v_max_i32_e32 v200, 0, v13
	v_fmac_f32_e32 v57, v68, v200
	v_max_i32_e32 v200, 0, v14
	v_fmac_f32_e32 v56, v68, v200
	v_max_i32_e32 v200, 0, v15
	v_fmac_f32_e32 v55, v68, v200
	v_max_i32_e32 v200, 0, v16
	v_fmac_f32_e32 v54, v68, v200
	v_max_i32_e32 v200, 0, v17
	v_fmac_f32_e32 v53, v68, v200
	v_max_i32_e32 v200, 0, v180
	v_fmac_f32_e32 v136, v69, v200
	v_max_i32_e32 v200, 0, v181
	v_fmac_f32_e32 v135, v69, v200
	v_max_i32_e32 v200, 0, v182
	v_fmac_f32_e32 v134, v69, v200
	v_max_i32_e32 v200, 0, v183
	v_fmac_f32_e32 v65, v69, v200
	v_max_i32_e32 v200, 0, v184
	v_fmac_f32_e32 v64, v69, v200
	v_max_i32_e32 v200, 0, v185
	v_fmac_f32_e32 v63, v69, v200
	v_max_i32_e32 v200, 0, v186
	v_fmac_f32_e32 v62, v69, v200
	v_max_i32_e32 v200, 0, v187
	v_fmac_f32_e32 v61, v69, v200
	v_max_i32_e32 v200, 0, v188
	v_fmac_f32_e32 v60, v69, v200
	v_max_i32_e32 v200, 0, v189
	v_fmac_f32_e32 v59, v69, v200
	v_max_i32_e32 v200, 0, v190
	v_fmac_f32_e32 v58, v69, v200
	v_max_i32_e32 v200, 0, v191
	v_fmac_f32_e32 v57, v69, v200
	v_max_i32_e32 v200, 0, v192
	v_fmac_f32_e32 v56, v69, v200
	v_max_i32_e32 v200, 0, v193
	v_fmac_f32_e32 v55, v69, v200
	v_max_i32_e32 v200, 0, v194
	v_fmac_f32_e32 v54, v69, v200
	v_max_i32_e32 v200, 0, v195
	v_fmac_f32_e32 v53, v69, v200
	s_cbranch_vccz .LBB0_714
; #define LAS __attribute__((address_space(3)))
; __device__ __forceinline__ int crow(int r, int hi) { return (r & 3) + 8 * (r >> 2) + 4 * hi; }
; __device__ __forceinline__ int ibin_u(unsigned u) {
;     const int a = (int)u >> 20;
;     return imed3(-953 - a, 0, 159) + imed3(a - 936, 0, 158) + imed3((int)u, -160, 1) + 160;
; }
; __device__ __forceinline__ int ibin_u_m160(unsigned u) {
;     const int a = (int)u >> 20;
;     return imed3(-953 - a, 0, 159) + imed3(a - 936, 0, 158) + imed3((int)u, -160, 1);
; }
; template <int PASS, bool DIAG> __device__ __forceinline__ void idx_half(unsigned& bits, unsigned& ebits, const f32x16& sc, int sbase, int tq, int r32, int hi, unsigned khi, unsigned klo, bool cand, LAS unsigned char* L) {
;     ...
;         LAS unsigned* H = (LAS unsigned*)(L + IL_HIST) + r32 * HSTR + 160;
; #pragma unroll
;         for (int r = 0; r < 16; ++r) { int b = ibin_u_m160(__float_as_uint(sc[r] + 0.0f)); asm("" : "+v"(b));
;             if (!DIAG || crow(r, 0) <= d) __hip_atomic_fetch_add(H + b, 1u, __ATOMIC_RELAXED, __HIP_MEMORY_SCOPE_WORKGROUP); }
	v_add_f32_e32 v2, 0, v136
	v_ashrrev_i32_e32 v3, 20, v2
	v_sub_u32_e32 v4, 0xfffffc47, v3
	v_med3_i32 v3, v3, s88, v233
	v_med3_i32 v2, v2, s89, 1
	v_med3_i32 v4, v4, 0, v232
	v_add_u32_e32 v2, v2, v3
	v_add3_u32 v2, v2, v4, s92
	s_nop 0
	v_lshl_add_u32 v2, v2, 2, v0
	ds_add_u32 v2, v229 offset:1152
	v_add_f32_e32 v2, 0, v135
	v_ashrrev_i32_e32 v3, 20, v2
	v_sub_u32_e32 v4, 0xfffffc47, v3
	v_med3_i32 v3, v3, s88, v233
	v_med3_i32 v2, v2, s89, 1
	v_med3_i32 v4, v4, 0, v232
	v_add_u32_e32 v2, v2, v3
	v_add3_u32 v2, v2, v4, s92
	s_mov_b64 s[16:17], -1
	v_lshl_add_u32 v2, v2, 2, v0
	ds_add_u32 v2, v229 offset:1152
	v_add_f32_e32 v2, 0, v134
	v_ashrrev_i32_e32 v3, 20, v2
	v_sub_u32_e32 v4, 0xfffffc47, v3
	v_med3_i32 v3, v3, s88, v233
	v_med3_i32 v2, v2, s89, 1
	v_med3_i32 v4, v4, 0, v232
	v_add_u32_e32 v2, v2, v3
	v_add3_u32 v2, v2, v4, s92
	s_nop 0
	v_lshl_add_u32 v2, v2, 2, v0
	ds_add_u32 v2, v229 offset:1152
	v_add_f32_e32 v2, 0, v65
	v_ashrrev_i32_e32 v3, 20, v2
	v_sub_u32_e32 v4, 0xfffffc47, v3
	v_med3_i32 v3, v3, s88, v233
	v_med3_i32 v2, v2, s89, 1
	v_med3_i32 v4, v4, 0, v232
	v_add_u32_e32 v2, v2, v3
	v_add3_u32 v2, v2, v4, s92
	s_nop 0
	v_lshl_add_u32 v2, v2, 2, v0
	ds_add_u32 v2, v229 offset:1152
	v_add_f32_e32 v2, 0, v64
	v_ashrrev_i32_e32 v3, 20, v2
	v_sub_u32_e32 v4, 0xfffffc47, v3
	v_med3_i32 v3, v3, s88, v233
	v_med3_i32 v2, v2, s89, 1
	v_med3_i32 v4, v4, 0, v232
	v_add_u32_e32 v2, v2, v3
	v_add3_u32 v2, v2, v4, s92
	s_nop 0
	v_lshl_add_u32 v2, v2, 2, v0
	ds_add_u32 v2, v229 offset:1152
	v_add_f32_e32 v2, 0, v63
	v_ashrrev_i32_e32 v3, 20, v2
	v_sub_u32_e32 v4, 0xfffffc47, v3
	v_med3_i32 v3, v3, s88, v233
	v_med3_i32 v2, v2, s89, 1
	v_med3_i32 v4, v4, 0, v232
	v_add_u32_e32 v2, v2, v3
	v_add3_u32 v2, v2, v4, s92
	s_nop 0
	v_lshl_add_u32 v2, v2, 2, v0
	ds_add_u32 v2, v229 offset:1152
	v_add_f32_e32 v2, 0, v62
	v_ashrrev_i32_e32 v3, 20, v2
	v_sub_u32_e32 v4, 0xfffffc47, v3
	v_med3_i32 v3, v3, s88, v233
	v_med3_i32 v2, v2, s89, 1
	v_med3_i32 v4, v4, 0, v232
	v_add_u32_e32 v2, v2, v3
	v_add3_u32 v2, v2, v4, s92
	s_nop 0
	v_lshl_add_u32 v2, v2, 2, v0
	ds_add_u32 v2, v229 offset:1152
	v_add_f32_e32 v2, 0, v61
	v_ashrrev_i32_e32 v3, 20, v2
	v_sub_u32_e32 v4, 0xfffffc47, v3
	v_med3_i32 v3, v3, s88, v233
	v_med3_i32 v2, v2, s89, 1
	v_med3_i32 v4, v4, 0, v232
	v_add_u32_e32 v2, v2, v3
	v_add3_u32 v2, v2, v4, s92
	s_nop 0
	v_lshl_add_u32 v2, v2, 2, v0
	ds_add_u32 v2, v229 offset:1152
	v_add_f32_e32 v2, 0, v60
	v_ashrrev_i32_e32 v3, 20, v2
	v_sub_u32_e32 v4, 0xfffffc47, v3
	v_med3_i32 v3, v3, s88, v233
	v_med3_i32 v2, v2, s89, 1
	v_med3_i32 v4, v4, 0, v232
	v_add_u32_e32 v2, v2, v3
	v_add3_u32 v2, v2, v4, s92
	s_nop 0
	v_lshl_add_u32 v2, v2, 2, v0
	ds_add_u32 v2, v229 offset:1152
	v_add_f32_e32 v2, 0, v59
	v_ashrrev_i32_e32 v3, 20, v2
	v_sub_u32_e32 v4, 0xfffffc47, v3
	v_med3_i32 v3, v3, s88, v233
	v_med3_i32 v2, v2, s89, 1
	v_med3_i32 v4, v4, 0, v232
	v_add_u32_e32 v2, v2, v3
	v_add3_u32 v2, v2, v4, s92
	s_nop 0
	v_lshl_add_u32 v2, v2, 2, v0
	ds_add_u32 v2, v229 offset:1152
	v_add_f32_e32 v2, 0, v58
	v_ashrrev_i32_e32 v3, 20, v2
	v_sub_u32_e32 v4, 0xfffffc47, v3
	v_med3_i32 v3, v3, s88, v233
	v_med3_i32 v2, v2, s89, 1
	v_med3_i32 v4, v4, 0, v232
	v_add_u32_e32 v2, v2, v3
	v_add3_u32 v2, v2, v4, s92
	s_nop 0
	v_lshl_add_u32 v2, v2, 2, v0
	ds_add_u32 v2, v229 offset:1152
	v_add_f32_e32 v2, 0, v57
	v_ashrrev_i32_e32 v3, 20, v2
	v_sub_u32_e32 v4, 0xfffffc47, v3
	v_med3_i32 v3, v3, s88, v233
	v_med3_i32 v2, v2, s89, 1
	v_med3_i32 v4, v4, 0, v232
	v_add_u32_e32 v2, v2, v3
	v_add3_u32 v2, v2, v4, s92
	s_nop 0
	v_lshl_add_u32 v2, v2, 2, v0
	ds_add_u32 v2, v229 offset:1152
	v_add_f32_e32 v2, 0, v56
	v_ashrrev_i32_e32 v3, 20, v2
	v_sub_u32_e32 v4, 0xfffffc47, v3
	v_med3_i32 v3, v3, s88, v233
	v_med3_i32 v2, v2, s89, 1
	v_med3_i32 v4, v4, 0, v232
	v_add_u32_e32 v2, v2, v3
	v_add3_u32 v2, v2, v4, s92
	s_nop 0
	v_lshl_add_u32 v2, v2, 2, v0
	ds_add_u32 v2, v229 offset:1152
	v_add_f32_e32 v2, 0, v55
	v_ashrrev_i32_e32 v3, 20, v2
	v_sub_u32_e32 v4, 0xfffffc47, v3
	v_med3_i32 v3, v3, s88, v233
	v_med3_i32 v2, v2, s89, 1
	v_med3_i32 v4, v4, 0, v232
	v_add_u32_e32 v2, v2, v3
	v_add3_u32 v2, v2, v4, s92
	s_nop 0
	v_lshl_add_u32 v2, v2, 2, v0
	ds_add_u32 v2, v229 offset:1152
	v_add_f32_e32 v2, 0, v54
	v_ashrrev_i32_e32 v3, 20, v2
	v_sub_u32_e32 v4, 0xfffffc47, v3
	v_med3_i32 v3, v3, s88, v233
	v_med3_i32 v2, v2, s89, 1
	v_med3_i32 v4, v4, 0, v232
	v_add_u32_e32 v2, v2, v3
	v_add3_u32 v2, v2, v4, s92
	s_nop 0
	v_lshl_add_u32 v2, v2, 2, v0
	ds_add_u32 v2, v229 offset:1152
	v_add_f32_e32 v2, 0, v53
	v_ashrrev_i32_e32 v3, 20, v2
	v_sub_u32_e32 v4, 0xfffffc47, v3
	v_med3_i32 v3, v3, s88, v233
	v_med3_i32 v2, v2, s89, 1
	v_med3_i32 v4, v4, 0, v232
	v_add_u32_e32 v2, v2, v3
	v_add3_u32 v2, v2, v4, s92
	s_cbranch_execz .LBB0_715
	s_branch .LBB0_746

; __device__ __forceinline__ float relu_i(float p) { const int i = __float_as_int(p); return __int_as_float(i > 0 ? i : 0); }
; __device__ __forceinline__ void idx_scores_k(f32x16& sc, const bf16x8 (&kf)[4], const bf16x8 (&qf)[16], const f32x4& w) {
;     f32x16 p0 = f32x16{}, p1 = f32x16{};
; #pragma unroll
;     for (int d0 = 0; d0 < 4; ++d0) p0 = __builtin_amdgcn_mfma_f32_32x32x16_bf16(kf[d0], qf[d0], p0, 0, 0, 0);
; #pragma unroll
;     for (int d0 = 0; d0 < 4; ++d0) p1 = __builtin_amdgcn_mfma_f32_32x32x16_bf16(kf[d0], qf[4 + d0], p1, 0, 0, 0);
; #pragma unroll
;     for (int r = 0; r < 16; ++r) sc[r] = w[0] * relu_i(p0[r]);
;     p0 = f32x16{};
; #pragma unroll
;     for (int d0 = 0; d0 < 4; ++d0) p0 = __builtin_amdgcn_mfma_f32_32x32x16_bf16(kf[d0], qf[8 + d0], p0, 0, 0, 0);
; #pragma unroll
;     for (int r = 0; r < 16; ++r) sc[r] = fmaf(w[1], relu_i(p1[r]), sc[r]);
;     p1 = f32x16{};
; #pragma unroll
;     for (int d0 = 0; d0 < 4; ++d0) p1 = __builtin_amdgcn_mfma_f32_32x32x16_bf16(kf[d0], qf[12 + d0], p1, 0, 0, 0);
; #pragma unroll
;     for (int r = 0; r < 16; ++r) sc[r] = fmaf(w[2], relu_i(p0[r]), sc[r]);
; #pragma unroll
;     for (int r = 0; r < 16; ++r) sc[r] = fmaf(w[3], relu_i(p1[r]), sc[r]);
; }
; template <int PASS> __device__ __forceinline__ void idx_pass(const bf16_t* KIb, const bf16x8 (&qf)[16], const f32x4& w, int jd, int tq, int wid, int r32, int hi, unsigned khi, unsigned klo, bool cand, LAS unsigned char* L) {
;     ...
;         idx_scores_k(sc, kB, qf, w);
.LBB0_750:
	s_and_b64 vcc, exec, s[14:15]
	s_waitcnt vmcnt(3)
	v_mfma_f32_32x32x16_bf16 v[2:17], v[46:49], v[70:73], 0
	s_waitcnt vmcnt(2)
	v_mfma_f32_32x32x16_bf16 v[2:17], v[42:45], v[74:77], v[2:17]
	s_waitcnt vmcnt(1)
	v_mfma_f32_32x32x16_bf16 v[2:17], v[38:41], v[78:81], v[2:17]
	s_waitcnt vmcnt(0)
	v_mfma_f32_32x32x16_bf16 v[2:17], v[34:37], v[82:85], v[2:17]
	v_mfma_f32_32x32x16_bf16 v[180:195], v[46:49], v[86:89], 0
	v_mfma_f32_32x32x16_bf16 v[180:195], v[42:45], v[90:93], v[180:195]
	v_mfma_f32_32x32x16_bf16 v[180:195], v[38:41], v[94:97], v[180:195]
	v_mfma_f32_32x32x16_bf16 v[180:195], v[34:37], v[98:101], v[180:195]
	s_nop 7
	v_max_i32_e32 v200, 0, v2
	v_mul_f32_e32 v136, v66, v200
	v_max_i32_e32 v200, 0, v3
	v_mul_f32_e32 v135, v66, v200
	v_max_i32_e32 v200, 0, v4
	v_mul_f32_e32 v134, v66, v200
	v_max_i32_e32 v200, 0, v5
	v_mul_f32_e32 v65, v66, v200
	v_max_i32_e32 v200, 0, v6
	v_mul_f32_e32 v64, v66, v200
	v_max_i32_e32 v200, 0, v7
	v_mul_f32_e32 v63, v66, v200
	v_max_i32_e32 v200, 0, v8
	v_mul_f32_e32 v62, v66, v200
	v_max_i32_e32 v200, 0, v9
	v_mul_f32_e32 v61, v66, v200
	v_max_i32_e32 v200, 0, v10
	v_mul_f32_e32 v60, v66, v200
	v_max_i32_e32 v200, 0, v11
	v_mul_f32_e32 v59, v66, v200
	v_max_i32_e32 v200, 0, v12
	v_mul_f32_e32 v58, v66, v200
	v_max_i32_e32 v200, 0, v13
	v_mul_f32_e32 v57, v66, v200
	v_max_i32_e32 v200, 0, v14
	v_mul_f32_e32 v56, v66, v200
	v_max_i32_e32 v200, 0, v15
	v_mul_f32_e32 v55, v66, v200
	v_max_i32_e32 v200, 0, v16
	v_mul_f32_e32 v54, v66, v200
	v_max_i32_e32 v200, 0, v17
	v_mul_f32_e32 v53, v66, v200
	v_mfma_f32_32x32x16_bf16 v[2:17], v[46:49], v[102:105], 0
	v_mfma_f32_32x32x16_bf16 v[2:17], v[42:45], v[106:109], v[2:17]
	v_mfma_f32_32x32x16_bf16 v[2:17], v[38:41], v[110:113], v[2:17]
	v_mfma_f32_32x32x16_bf16 v[2:17], v[34:37], v[114:117], v[2:17]
	v_max_i32_e32 v200, 0, v180
	v_fmac_f32_e32 v136, v67, v200
	v_max_i32_e32 v200, 0, v181
	v_fmac_f32_e32 v135, v67, v200
	v_max_i32_e32 v200, 0, v182
	v_fmac_f32_e32 v134, v67, v200
	v_max_i32_e32 v200, 0, v183
	v_fmac_f32_e32 v65, v67, v200
	v_max_i32_e32 v200, 0, v184
	v_fmac_f32_e32 v64, v67, v200
	v_max_i32_e32 v200, 0, v185
	v_fmac_f32_e32 v63, v67, v200
	v_max_i32_e32 v200, 0, v186
	v_fmac_f32_e32 v62, v67, v200
	v_max_i32_e32 v200, 0, v187
	v_fmac_f32_e32 v61, v67, v200
	v_max_i32_e32 v200, 0, v188
	v_fmac_f32_e32 v60, v67, v200
	v_max_i32_e32 v200, 0, v189
	v_fmac_f32_e32 v59, v67, v200
	v_max_i32_e32 v200, 0, v190
	v_fmac_f32_e32 v58, v67, v200
	v_max_i32_e32 v200, 0, v191
	v_fmac_f32_e32 v57, v67, v200
	v_max_i32_e32 v200, 0, v192
	v_fmac_f32_e32 v56, v67, v200
	v_max_i32_e32 v200, 0, v193
	v_fmac_f32_e32 v55, v67, v200
	v_max_i32_e32 v200, 0, v194
	v_fmac_f32_e32 v54, v67, v200
	v_max_i32_e32 v200, 0, v195
	v_fmac_f32_e32 v53, v67, v200
	v_mfma_f32_32x32x16_bf16 v[180:195], v[46:49], v[118:121], 0
	v_mfma_f32_32x32x16_bf16 v[180:195], v[42:45], v[122:125], v[180:195]
	v_mfma_f32_32x32x16_bf16 v[180:195], v[38:41], v[126:129], v[180:195]
	v_mfma_f32_32x32x16_bf16 v[180:195], v[34:37], v[130:133], v[180:195]
	v_max_i32_e32 v200, 0, v2
	v_fmac_f32_e32 v136, v68, v200
	v_max_i32_e32 v200, 0, v3
	v_fmac_f32_e32 v135, v68, v200
	v_max_i32_e32 v200, 0, v4
	v_fmac_f32_e32 v134, v68, v200
	v_max_i32_e32 v200, 0, v5
	v_fmac_f32_e32 v65, v68, v200
	v_max_i32_e32 v200, 0, v6
	v_fmac_f32_e32 v64, v68, v200
	v_max_i32_e32 v200, 0, v7
	v_fmac_f32_e32 v63, v68, v200
	v_max_i32_e32 v200, 0, v8
	v_fmac_f32_e32 v62, v68, v200
	v_max_i32_e32 v200, 0, v9
	v_fmac_f32_e32 v61, v68, v200
	v_max_i32_e32 v200, 0, v10
	v_fmac_f32_e32 v60, v68, v200
	v_max_i32_e32 v200, 0, v11
	v_fmac_f32_e32 v59, v68, v200
	v_max_i32_e32 v200, 0, v12
	v_fmac_f32_e32 v58, v68, v200
	v_max_i32_e32 v200, 0, v13
	v_fmac_f32_e32 v57, v68, v200
	v_max_i32_e32 v200, 0, v14
	v_fmac_f32_e32 v56, v68, v200
	v_max_i32_e32 v200, 0, v15
	v_fmac_f32_e32 v55, v68, v200
	v_max_i32_e32 v200, 0, v16
	v_fmac_f32_e32 v54, v68, v200
	v_max_i32_e32 v200, 0, v17
	v_fmac_f32_e32 v53, v68, v200
	v_max_i32_e32 v200, 0, v180
	v_fmac_f32_e32 v136, v69, v200
	v_max_i32_e32 v200, 0, v181
	v_fmac_f32_e32 v135, v69, v200
	v_max_i32_e32 v200, 0, v182
	v_fmac_f32_e32 v134, v69, v200
	v_max_i32_e32 v200, 0, v183
	v_fmac_f32_e32 v65, v69, v200
	v_max_i32_e32 v200, 0, v184
	v_fmac_f32_e32 v64, v69, v200
	v_max_i32_e32 v200, 0, v185
	v_fmac_f32_e32 v63, v69, v200
	v_max_i32_e32 v200, 0, v186
	v_fmac_f32_e32 v62, v69, v200
	v_max_i32_e32 v200, 0, v187
	v_fmac_f32_e32 v61, v69, v200
	v_max_i32_e32 v200, 0, v188
	v_fmac_f32_e32 v60, v69, v200
	v_max_i32_e32 v200, 0, v189
	v_fmac_f32_e32 v59, v69, v200
	v_max_i32_e32 v200, 0, v190
	v_fmac_f32_e32 v58, v69, v200
	v_max_i32_e32 v200, 0, v191
	v_fmac_f32_e32 v57, v69, v200
	v_max_i32_e32 v200, 0, v192
	v_fmac_f32_e32 v56, v69, v200
	v_max_i32_e32 v200, 0, v193
	v_fmac_f32_e32 v55, v69, v200
	v_max_i32_e32 v200, 0, v194
	v_fmac_f32_e32 v54, v69, v200
	v_max_i32_e32 v200, 0, v195
	v_fmac_f32_e32 v53, v69, v200
	s_cbranch_vccz .LBB0_752
; #define LAS __attribute__((address_space(3)))
; __device__ __forceinline__ int crow(int r, int hi) { return (r & 3) + 8 * (r >> 2) + 4 * hi; }
; __device__ __forceinline__ int ibin_u(unsigned u) {
;     const int a = (int)u >> 20;
;     return imed3(-953 - a, 0, 159) + imed3(a - 936, 0, 158) + imed3((int)u, -160, 1) + 160;
; }
; __device__ __forceinline__ int ibin_u_m160(unsigned u) {
;     const int a = (int)u >> 20;
;     return imed3(-953 - a, 0, 159) + imed3(a - 936, 0, 158) + imed3((int)u, -160, 1);
; }
; template <int PASS, bool DIAG> __device__ __forceinline__ void idx_half(unsigned& bits, unsigned& ebits, const f32x16& sc, int sbase, int tq, int r32, int hi, unsigned khi, unsigned klo, bool cand, LAS unsigned char* L) {
;     ...
;         LAS unsigned* H = (LAS unsigned*)(L + IL_HIST) + r32 * HSTR + 160;
; #pragma unroll
;         for (int r = 0; r < 16; ++r) { int b = ibin_u_m160(__float_as_uint(sc[r] + 0.0f)); asm("" : "+v"(b));
;             if (!DIAG || crow(r, 0) <= d) __hip_atomic_fetch_add(H + b, 1u, __ATOMIC_RELAXED, __HIP_MEMORY_SCOPE_WORKGROUP); }
	v_add_f32_e32 v2, 0, v136
	v_ashrrev_i32_e32 v3, 20, v2
	v_sub_u32_e32 v4, 0xfffffc47, v3
	v_med3_i32 v3, v3, s88, v233
	v_med3_i32 v2, v2, s89, 1
	v_med3_i32 v4, v4, 0, v232
	v_add_u32_e32 v2, v2, v3
	v_add3_u32 v2, v2, v4, s92
	s_nop 0
	v_lshl_add_u32 v2, v2, 2, v0
	ds_add_u32 v2, v229 offset:1152
	v_add_f32_e32 v2, 0, v135
	v_ashrrev_i32_e32 v3, 20, v2
	v_sub_u32_e32 v4, 0xfffffc47, v3
	v_med3_i32 v3, v3, s88, v233
	v_med3_i32 v2, v2, s89, 1
	v_med3_i32 v4, v4, 0, v232
	v_add_u32_e32 v2, v2, v3
	v_add3_u32 v2, v2, v4, s92
	s_mov_b64 s[14:15], -1
	v_lshl_add_u32 v2, v2, 2, v0
	ds_add_u32 v2, v229 offset:1152
	v_add_f32_e32 v2, 0, v134
	v_ashrrev_i32_e32 v3, 20, v2
	v_sub_u32_e32 v4, 0xfffffc47, v3
	v_med3_i32 v3, v3, s88, v233
	v_med3_i32 v2, v2, s89, 1
	v_med3_i32 v4, v4, 0, v232
	v_add_u32_e32 v2, v2, v3
	v_add3_u32 v2, v2, v4, s92
	s_nop 0
	v_lshl_add_u32 v2, v2, 2, v0
	ds_add_u32 v2, v229 offset:1152
	v_add_f32_e32 v2, 0, v65
	v_ashrrev_i32_e32 v3, 20, v2
	v_sub_u32_e32 v4, 0xfffffc47, v3
	v_med3_i32 v3, v3, s88, v233
	v_med3_i32 v2, v2, s89, 1
	v_med3_i32 v4, v4, 0, v232
	v_add_u32_e32 v2, v2, v3
	v_add3_u32 v2, v2, v4, s92
	s_nop 0
	v_lshl_add_u32 v2, v2, 2, v0
	ds_add_u32 v2, v229 offset:1152
	v_add_f32_e32 v2, 0, v64
	v_ashrrev_i32_e32 v3, 20, v2
	v_sub_u32_e32 v4, 0xfffffc47, v3
	v_med3_i32 v3, v3, s88, v233
	v_med3_i32 v2, v2, s89, 1
	v_med3_i32 v4, v4, 0, v232
	v_add_u32_e32 v2, v2, v3
	v_add3_u32 v2, v2, v4, s92
	s_nop 0
	v_lshl_add_u32 v2, v2, 2, v0
	ds_add_u32 v2, v229 offset:1152
	v_add_f32_e32 v2, 0, v63
	v_ashrrev_i32_e32 v3, 20, v2
	v_sub_u32_e32 v4, 0xfffffc47, v3
	v_med3_i32 v3, v3, s88, v233
	v_med3_i32 v2, v2, s89, 1
	v_med3_i32 v4, v4, 0, v232
	v_add_u32_e32 v2, v2, v3
	v_add3_u32 v2, v2, v4, s92
	s_nop 0
	v_lshl_add_u32 v2, v2, 2, v0
	ds_add_u32 v2, v229 offset:1152
	v_add_f32_e32 v2, 0, v62
	v_ashrrev_i32_e32 v3, 20, v2
	v_sub_u32_e32 v4, 0xfffffc47, v3
	v_med3_i32 v3, v3, s88, v233
	v_med3_i32 v2, v2, s89, 1
	v_med3_i32 v4, v4, 0, v232
	v_add_u32_e32 v2, v2, v3
	v_add3_u32 v2, v2, v4, s92
	s_nop 0
	v_lshl_add_u32 v2, v2, 2, v0
	ds_add_u32 v2, v229 offset:1152
	v_add_f32_e32 v2, 0, v61
	v_ashrrev_i32_e32 v3, 20, v2
	v_sub_u32_e32 v4, 0xfffffc47, v3
	v_med3_i32 v3, v3, s88, v233
	v_med3_i32 v2, v2, s89, 1
	v_med3_i32 v4, v4, 0, v232
	v_add_u32_e32 v2, v2, v3
	v_add3_u32 v2, v2, v4, s92
	s_nop 0
	v_lshl_add_u32 v2, v2, 2, v0
	ds_add_u32 v2, v229 offset:1152
	v_add_f32_e32 v2, 0, v60
	v_ashrrev_i32_e32 v3, 20, v2
	v_sub_u32_e32 v4, 0xfffffc47, v3
	v_med3_i32 v3, v3, s88, v233
	v_med3_i32 v2, v2, s89, 1
	v_med3_i32 v4, v4, 0, v232
	v_add_u32_e32 v2, v2, v3
	v_add3_u32 v2, v2, v4, s92
	s_nop 0
	v_lshl_add_u32 v2, v2, 2, v0
	ds_add_u32 v2, v229 offset:1152
	v_add_f32_e32 v2, 0, v59
	v_ashrrev_i32_e32 v3, 20, v2
	v_sub_u32_e32 v4, 0xfffffc47, v3
	v_med3_i32 v3, v3, s88, v233
	v_med3_i32 v2, v2, s89, 1
	v_med3_i32 v4, v4, 0, v232
	v_add_u32_e32 v2, v2, v3
	v_add3_u32 v2, v2, v4, s92
	s_nop 0
	v_lshl_add_u32 v2, v2, 2, v0
	ds_add_u32 v2, v229 offset:1152
	v_add_f32_e32 v2, 0, v58
	v_ashrrev_i32_e32 v3, 20, v2
	v_sub_u32_e32 v4, 0xfffffc47, v3
	v_med3_i32 v3, v3, s88, v233
	v_med3_i32 v2, v2, s89, 1
	v_med3_i32 v4, v4, 0, v232
	v_add_u32_e32 v2, v2, v3
	v_add3_u32 v2, v2, v4, s92
	s_nop 0
	v_lshl_add_u32 v2, v2, 2, v0
	ds_add_u32 v2, v229 offset:1152
	v_add_f32_e32 v2, 0, v57
	v_ashrrev_i32_e32 v3, 20, v2
	v_sub_u32_e32 v4, 0xfffffc47, v3
	v_med3_i32 v3, v3, s88, v233
	v_med3_i32 v2, v2, s89, 1
	v_med3_i32 v4, v4, 0, v232
	v_add_u32_e32 v2, v2, v3
	v_add3_u32 v2, v2, v4, s92
	s_nop 0
	v_lshl_add_u32 v2, v2, 2, v0
	ds_add_u32 v2, v229 offset:1152
	v_add_f32_e32 v2, 0, v56
	v_ashrrev_i32_e32 v3, 20, v2
	v_sub_u32_e32 v4, 0xfffffc47, v3
	v_med3_i32 v3, v3, s88, v233
	v_med3_i32 v2, v2, s89, 1
	v_med3_i32 v4, v4, 0, v232
	v_add_u32_e32 v2, v2, v3
	v_add3_u32 v2, v2, v4, s92
	s_nop 0
	v_lshl_add_u32 v2, v2, 2, v0
	ds_add_u32 v2, v229 offset:1152
	v_add_f32_e32 v2, 0, v55
	v_ashrrev_i32_e32 v3, 20, v2
	v_sub_u32_e32 v4, 0xfffffc47, v3
	v_med3_i32 v3, v3, s88, v233
	v_med3_i32 v2, v2, s89, 1
	v_med3_i32 v4, v4, 0, v232
	v_add_u32_e32 v2, v2, v3
	v_add3_u32 v2, v2, v4, s92
	s_nop 0
	v_lshl_add_u32 v2, v2, 2, v0
	ds_add_u32 v2, v229 offset:1152
	v_add_f32_e32 v2, 0, v54
	v_ashrrev_i32_e32 v3, 20, v2
	v_sub_u32_e32 v4, 0xfffffc47, v3
	v_med3_i32 v3, v3, s88, v233
	v_med3_i32 v2, v2, s89, 1
	v_med3_i32 v4, v4, 0, v232
	v_add_u32_e32 v2, v2, v3
	v_add3_u32 v2, v2, v4, s92
	s_nop 0
	v_lshl_add_u32 v2, v2, 2, v0
	ds_add_u32 v2, v229 offset:1152
	v_add_f32_e32 v2, 0, v53
	v_ashrrev_i32_e32 v3, 20, v2
	v_sub_u32_e32 v4, 0xfffffc47, v3
	v_med3_i32 v3, v3, s88, v233
	v_med3_i32 v2, v2, s89, 1
	v_med3_i32 v4, v4, 0, v232
	v_add_u32_e32 v2, v2, v3
	v_add3_u32 v3, v2, v4, s92
	s_cbranch_execz .LBB0_753
	s_branch .LBB0_784

; #define LAS __attribute__((address_space(3)))
; __device__ __forceinline__ unsigned fkey2(float v) { const unsigned u = __float_as_uint(v + 0.0f); return u ^ ((unsigned)((int)u >> 31) | 0x80000000u); }
; __device__ __forceinline__ int ibin_u(unsigned u) {
;     const int a = (int)u >> 20;
;     return imed3(-953 - a, 0, 159) + imed3(a - 936, 0, 158) + imed3((int)u, -160, 1) + 160;
; }
; __device__ __forceinline__ int ibin_u_m160(unsigned u) {
;     const int a = (int)u >> 20;
;     return imed3(-953 - a, 0, 159) + imed3(a - 936, 0, 158) + imed3((int)u, -160, 1);
; }
; template <int PASS> __device__ __forceinline__ void idx_pass(const bf16_t* KIb, const bf16x8 (&qf)[16], const f32x4& w, int jd, int tq, int wid, int r32, int hi, unsigned khi, unsigned klo, bool cand, LAS unsigned char* L) {
;     bf16x8 kA[4], kB[4];
;     int j = wid;
;     if (j <= jd) idx_loadk(kA, KIb + (size_t)(j * 64) * 64, r32, hi);
.LBB0_1062:
	s_movk_i32 s0, 0x5fc
	v_mad_u32_u24 v136, v222, s0, v221
	s_lshl_b32 s0, s64, 3
	v_lshlrev_b32_e32 v0, 7, v222
	s_add_i32 s0, s0, 0
	v_lshl_add_u64 v[2:3], s[38:39], 0, v[0:1]
	v_lshlrev_b32_e32 v0, 4, v223
	v_lshlrev_b32_e32 v137, 2, v223
	s_add_i32 s0, s0, 0xc200
	v_lshl_add_u64 v[50:51], v[2:3], 0, v[0:1]
	v_xor_b32_e32 v138, 0xffff, v137
	v_lshl_add_u32 v139, v222, 9, s0
	s_lshl_b32 s0, s64, 6
	v_add_u32_e32 v0, s62, v222
	v_cmp_gt_u32_e64 s[12:13], 32, v224
	s_add_i32 s16, s0, 0x200
	s_add_i32 s44, s64, 8
	s_sub_i32 s45, 0, s0
	v_sub_u32_e32 v140, 0, v137
	v_sub_u32_e32 v141, v0, v137
	s_sub_i32 s46, 0, s65
	v_mov_b32_e32 v142, v138
	v_not_b32_e32 v252, v134
	v_ashrrev_i32_e32 v252, 31, v252
	v_bitop3_b32 v253, v252, v134, s85 bitop3:0x36
	v_cmp_eq_u32_e32 vcc, 0, v134
	v_mov_b32_e32 v252, 0xff800000
	s_nop 0
	v_cndmask_b32_e32 v164, v253, v252, vcc
	v_not_b32_e32 v252, v135
	v_ashrrev_i32_e32 v252, 31, v252
	v_bitop3_b32 v253, v252, v135, s85 bitop3:0x36
	v_cmp_eq_u32_e32 vcc, 0, v135
	v_mov_b32_e32 v252, 0xff800000
	s_nop 0
	v_cndmask_b32_e32 v165, v253, v252, vcc
	s_branch .LBB0_1064

; __device__ __forceinline__ float relu_i(float p) { const int i = __float_as_int(p); return __int_as_float(i > 0 ? i : 0); }
; __device__ __forceinline__ void idx_scores_k(f32x16& sc, const bf16x8 (&kf)[4], const bf16x8 (&qf)[16], const f32x4& w) {
;     f32x16 p0 = f32x16{}, p1 = f32x16{};
; #pragma unroll
;     for (int d0 = 0; d0 < 4; ++d0) p0 = __builtin_amdgcn_mfma_f32_32x32x16_bf16(kf[d0], qf[d0], p0, 0, 0, 0);
; #pragma unroll
;     for (int d0 = 0; d0 < 4; ++d0) p1 = __builtin_amdgcn_mfma_f32_32x32x16_bf16(kf[d0], qf[4 + d0], p1, 0, 0, 0);
; #pragma unroll
;     for (int r = 0; r < 16; ++r) sc[r] = w[0] * relu_i(p0[r]);
;     p0 = f32x16{};
; #pragma unroll
;     for (int d0 = 0; d0 < 4; ++d0) p0 = __builtin_amdgcn_mfma_f32_32x32x16_bf16(kf[d0], qf[8 + d0], p0, 0, 0, 0);
; #pragma unroll
;     for (int r = 0; r < 16; ++r) sc[r] = fmaf(w[1], relu_i(p1[r]), sc[r]);
;     p1 = f32x16{};
; #pragma unroll
;     for (int d0 = 0; d0 < 4; ++d0) p1 = __builtin_amdgcn_mfma_f32_32x32x16_bf16(kf[d0], qf[12 + d0], p1, 0, 0, 0);
; #pragma unroll
;     for (int r = 0; r < 16; ++r) sc[r] = fmaf(w[2], relu_i(p0[r]), sc[r]);
; #pragma unroll
;     for (int r = 0; r < 16; ++r) sc[r] = fmaf(w[3], relu_i(p1[r]), sc[r]);
; }
; template <int PASS> __device__ __forceinline__ void idx_pass(const bf16_t* KIb, const bf16x8 (&qf)[16], const f32x4& w, int jd, int tq, int wid, int r32, int hi, unsigned khi, unsigned klo, bool cand, LAS unsigned char* L) {
;     ...
;     for (; j <= jd; j += 8) {
;         const bool diag = (j == jd);
;         idx_loadk(kB, KIb + (size_t)(j * 64 + 32) * 64, r32, hi);
;         f32x16 sc; idx_scores_k(sc, kA, qf, w);
;         unsigned lo, elo, hw, ehw;
;         if (diag) idx_half<PASS, true>(lo, elo, sc, j * 64, tq, r32, hi, khi, klo, cand, L); else idx_half<PASS, false>(lo, elo, sc, j * 64, tq, r32, hi, khi, klo, cand, L);
.LBB0_1064:
	s_add_i32 s0, s46, s44
	s_cmp_lg_u32 s0, 8
	s_cselect_b64 s[18:19], -1, 0
	s_add_i32 s0, s16, 0xfffffe20
	s_ashr_i32 s1, s0, 31
	s_lshl_b64 s[0:1], s[0:1], 7
	v_lshl_add_u64 v[2:3], v[50:51], 0, s[0:1]
	global_load_dwordx4 v[46:49], v[2:3], off
	global_load_dwordx4 v[42:45], v[2:3], off offset:32
	global_load_dwordx4 v[38:41], v[2:3], off offset:64
	global_load_dwordx4 v[34:37], v[2:3], off offset:96
	s_mov_b64 s[14:15], -1
	s_and_b64 vcc, exec, s[18:19]
	s_waitcnt vmcnt(7)
	v_mfma_f32_32x32x16_bf16 v[2:17], v[18:21], v[70:73], 0
	s_waitcnt vmcnt(6)
	v_mfma_f32_32x32x16_bf16 v[2:17], v[22:25], v[74:77], v[2:17]
	s_waitcnt vmcnt(5)
	v_mfma_f32_32x32x16_bf16 v[2:17], v[26:29], v[78:81], v[2:17]
	s_waitcnt vmcnt(4)
	v_mfma_f32_32x32x16_bf16 v[2:17], v[30:33], v[82:85], v[2:17]
	v_mfma_f32_32x32x16_bf16 v[180:195], v[18:21], v[86:89], 0
	v_mfma_f32_32x32x16_bf16 v[180:195], v[22:25], v[90:93], v[180:195]
	v_mfma_f32_32x32x16_bf16 v[180:195], v[26:29], v[94:97], v[180:195]
	v_mfma_f32_32x32x16_bf16 v[180:195], v[30:33], v[98:101], v[180:195]
	s_nop 7
	v_max_i32_e32 v200, 0, v2
	v_mul_f32_e32 v144, v66, v200
	v_max_i32_e32 v200, 0, v3
	v_mul_f32_e32 v145, v66, v200
	v_max_i32_e32 v200, 0, v4
	v_mul_f32_e32 v146, v66, v200
	v_max_i32_e32 v200, 0, v5
	v_mul_f32_e32 v147, v66, v200
	v_max_i32_e32 v200, 0, v6
	v_mul_f32_e32 v148, v66, v200
	v_max_i32_e32 v200, 0, v7
	v_mul_f32_e32 v149, v66, v200
	v_max_i32_e32 v200, 0, v8
	v_mul_f32_e32 v150, v66, v200
	v_max_i32_e32 v200, 0, v9
	v_mul_f32_e32 v151, v66, v200
	v_max_i32_e32 v200, 0, v10
	v_mul_f32_e32 v152, v66, v200
	v_max_i32_e32 v200, 0, v11
	v_mul_f32_e32 v153, v66, v200
	v_max_i32_e32 v200, 0, v12
	v_mul_f32_e32 v154, v66, v200
	v_max_i32_e32 v200, 0, v13
	v_mul_f32_e32 v155, v66, v200
	v_max_i32_e32 v200, 0, v14
	v_mul_f32_e32 v156, v66, v200
	v_max_i32_e32 v200, 0, v15
	v_mul_f32_e32 v157, v66, v200
	v_max_i32_e32 v200, 0, v16
	v_mul_f32_e32 v158, v66, v200
	v_max_i32_e32 v200, 0, v17
	v_mul_f32_e32 v159, v66, v200
	v_mfma_f32_32x32x16_bf16 v[2:17], v[18:21], v[102:105], 0
	v_mfma_f32_32x32x16_bf16 v[2:17], v[22:25], v[106:109], v[2:17]
	v_mfma_f32_32x32x16_bf16 v[2:17], v[26:29], v[110:113], v[2:17]
	v_mfma_f32_32x32x16_bf16 v[2:17], v[30:33], v[114:117], v[2:17]
	v_max_i32_e32 v200, 0, v180
	v_fmac_f32_e32 v144, v67, v200
	v_max_i32_e32 v200, 0, v181
	v_fmac_f32_e32 v145, v67, v200
	v_max_i32_e32 v200, 0, v182
	v_fmac_f32_e32 v146, v67, v200
	v_max_i32_e32 v200, 0, v183
	v_fmac_f32_e32 v147, v67, v200
	v_max_i32_e32 v200, 0, v184
	v_fmac_f32_e32 v148, v67, v200
	v_max_i32_e32 v200, 0, v185
	v_fmac_f32_e32 v149, v67, v200
	v_max_i32_e32 v200, 0, v186
	v_fmac_f32_e32 v150, v67, v200
	v_max_i32_e32 v200, 0, v187
	v_fmac_f32_e32 v151, v67, v200
	v_max_i32_e32 v200, 0, v188
	v_fmac_f32_e32 v152, v67, v200
	v_max_i32_e32 v200, 0, v189
	v_fmac_f32_e32 v153, v67, v200
	v_max_i32_e32 v200, 0, v190
	v_fmac_f32_e32 v154, v67, v200
	v_max_i32_e32 v200, 0, v191
	v_fmac_f32_e32 v155, v67, v200
	v_max_i32_e32 v200, 0, v192
	v_fmac_f32_e32 v156, v67, v200
	v_max_i32_e32 v200, 0, v193
	v_fmac_f32_e32 v157, v67, v200
	v_max_i32_e32 v200, 0, v194
	v_fmac_f32_e32 v158, v67, v200
	v_max_i32_e32 v200, 0, v195
	v_fmac_f32_e32 v159, v67, v200
	v_mfma_f32_32x32x16_bf16 v[180:195], v[18:21], v[118:121], 0
	v_mfma_f32_32x32x16_bf16 v[180:195], v[22:25], v[122:125], v[180:195]
	v_mfma_f32_32x32x16_bf16 v[180:195], v[26:29], v[126:129], v[180:195]
	v_mfma_f32_32x32x16_bf16 v[180:195], v[30:33], v[130:133], v[180:195]
	v_max_i32_e32 v200, 0, v2
	v_fmac_f32_e32 v144, v68, v200
	v_max_i32_e32 v200, 0, v3
	v_fmac_f32_e32 v145, v68, v200
	v_max_i32_e32 v200, 0, v4
	v_fmac_f32_e32 v146, v68, v200
	v_max_i32_e32 v200, 0, v5
	v_fmac_f32_e32 v147, v68, v200
	v_max_i32_e32 v200, 0, v6
	v_fmac_f32_e32 v148, v68, v200
	v_max_i32_e32 v200, 0, v7
	v_fmac_f32_e32 v149, v68, v200
	v_max_i32_e32 v200, 0, v8
	v_fmac_f32_e32 v150, v68, v200
	v_max_i32_e32 v200, 0, v9
	v_fmac_f32_e32 v151, v68, v200
	v_max_i32_e32 v200, 0, v10
	v_fmac_f32_e32 v152, v68, v200
	v_max_i32_e32 v200, 0, v11
	v_fmac_f32_e32 v153, v68, v200
	v_max_i32_e32 v200, 0, v12
	v_fmac_f32_e32 v154, v68, v200
	v_max_i32_e32 v200, 0, v13
	v_fmac_f32_e32 v155, v68, v200
	v_max_i32_e32 v200, 0, v14
	v_fmac_f32_e32 v156, v68, v200
	v_max_i32_e32 v200, 0, v15
	v_fmac_f32_e32 v157, v68, v200
	v_max_i32_e32 v200, 0, v16
	v_fmac_f32_e32 v158, v68, v200
	v_max_i32_e32 v200, 0, v17
	v_fmac_f32_e32 v159, v68, v200
	v_max_i32_e32 v200, 0, v180
	v_fmac_f32_e32 v144, v69, v200
	v_max_i32_e32 v200, 0, v181
	v_fmac_f32_e32 v145, v69, v200
	v_max_i32_e32 v200, 0, v182
	v_fmac_f32_e32 v146, v69, v200
	v_max_i32_e32 v200, 0, v183
	v_fmac_f32_e32 v147, v69, v200
	v_max_i32_e32 v200, 0, v184
	v_fmac_f32_e32 v148, v69, v200
	v_max_i32_e32 v200, 0, v185
	v_fmac_f32_e32 v149, v69, v200
	v_max_i32_e32 v200, 0, v186
	v_fmac_f32_e32 v150, v69, v200
	v_max_i32_e32 v200, 0, v187
	v_fmac_f32_e32 v151, v69, v200
	v_max_i32_e32 v200, 0, v188
	v_fmac_f32_e32 v152, v69, v200
	v_max_i32_e32 v200, 0, v189
	v_fmac_f32_e32 v153, v69, v200
	v_max_i32_e32 v200, 0, v190
	v_fmac_f32_e32 v154, v69, v200
	v_max_i32_e32 v200, 0, v191
	v_fmac_f32_e32 v155, v69, v200
	v_max_i32_e32 v200, 0, v192
	v_fmac_f32_e32 v156, v69, v200
	v_max_i32_e32 v200, 0, v193
	v_fmac_f32_e32 v157, v69, v200
	v_max_i32_e32 v200, 0, v194
	v_fmac_f32_e32 v158, v69, v200
	v_max_i32_e32 v200, 0, v195
	v_fmac_f32_e32 v159, v69, v200
	s_cbranch_vccz .LBB0_1263
; #define LAS __attribute__((address_space(3)))
; __device__ __forceinline__ int crow(int r, int hi) { return (r & 3) + 8 * (r >> 2) + 4 * hi; }
; __device__ __forceinline__ unsigned fkey2(float v) { const unsigned u = __float_as_uint(v + 0.0f); return u ^ ((unsigned)((int)u >> 31) | 0x80000000u); }
; __device__ __forceinline__ void shl_ge(unsigned& acc, unsigned key, unsigned thr) { asm("v_cmp_ge_u32 vcc, %1, %2\n\tv_addc_co_u32 %0, vcc, %0, %0, vcc" : "+v"(acc) : "v"(key), "v"(thr) : "vcc"); }
; __device__ __forceinline__ unsigned spread4(unsigned x) { return (x & 0xFu) | ((x & 0xF0u) << 4) | ((x & 0xF00u) << 8) | ((x & 0xF000u) << 12); }
; template <int PASS, bool DIAG> __device__ __forceinline__ void idx_half(unsigned& bits, unsigned& ebits, const f32x16& sc, int sbase, int tq, int r32, int hi, unsigned khi, unsigned klo, bool cand, LAS unsigned char* L) {
;     ...
;         unsigned hb = 0u, lb = 0u;
; #pragma unroll
;         for (int r = 15; r >= 0; --r) { const unsigned key = fkey2(sc[r]); shl_ge(hb, key, khi); shl_ge(lb, key, klo); }
;         bits = spread4(hb); ebits = spread4(lb & ~hb);
;         if (DIAG) { const unsigned vm = d < 0 ? 0u : (d >= 31 ? 0xFFFFFFFFu : ((2u << d) - 1u)); bits &= vm; ebits &= vm; }
;         if (cand && ebits != 0u) {
;             unsigned slot = __hip_atomic_fetch_add((LAS unsigned*)(L + IL_CNT) + r32, (unsigned)__builtin_popcount(ebits), __ATOMIC_RELAXED, __HIP_MEMORY_SCOPE_WORKGROUP);
; #pragma unroll
;             for (int r = 0; r < 16; ++r) if ((ebits >> crow(r, 0)) & 1u) { const int s = sbase + crow(r, hi);
;                 if (slot < (unsigned)IDX_CAP) ((LAS unsigned long long*)(L + IL_CAND))[r32 * IDX_CAP + slot] = ((unsigned long long)fkey2(sc[r]) << 16) | (unsigned long long)(0xFFFFu - (unsigned)s);
;                 ++slot; }
	v_mov_b32_e32 v160, 0
	v_mov_b32_e32 v5, 0
	v_cmp_ge_f32 vcc, v159, v165
	v_addc_co_u32 v160, vcc, v160, v160, vcc
	v_cmp_ge_f32 vcc, v159, v164
	v_addc_co_u32 v5, vcc, v5, v5, vcc
	v_cmp_ge_f32 vcc, v158, v165
	v_addc_co_u32 v160, vcc, v160, v160, vcc
	v_cmp_ge_f32 vcc, v158, v164
	v_addc_co_u32 v5, vcc, v5, v5, vcc
	v_cmp_ge_f32 vcc, v157, v165
	v_addc_co_u32 v160, vcc, v160, v160, vcc
	v_cmp_ge_f32 vcc, v157, v164
	v_addc_co_u32 v5, vcc, v5, v5, vcc
	v_cmp_ge_f32 vcc, v156, v165
	v_addc_co_u32 v160, vcc, v160, v160, vcc
	v_cmp_ge_f32 vcc, v156, v164
	v_addc_co_u32 v5, vcc, v5, v5, vcc
	v_cmp_ge_f32 vcc, v155, v165
	v_addc_co_u32 v160, vcc, v160, v160, vcc
	v_cmp_ge_f32 vcc, v155, v164
	v_addc_co_u32 v5, vcc, v5, v5, vcc
	v_cmp_ge_f32 vcc, v154, v165
	v_addc_co_u32 v160, vcc, v160, v160, vcc
	v_cmp_ge_f32 vcc, v154, v164
	v_addc_co_u32 v5, vcc, v5, v5, vcc
	v_cmp_ge_f32 vcc, v153, v165
	v_addc_co_u32 v160, vcc, v160, v160, vcc
	v_cmp_ge_f32 vcc, v153, v164
	v_addc_co_u32 v5, vcc, v5, v5, vcc
	v_cmp_ge_f32 vcc, v152, v165
	v_addc_co_u32 v160, vcc, v160, v160, vcc
	v_cmp_ge_f32 vcc, v152, v164
	v_addc_co_u32 v5, vcc, v5, v5, vcc
	v_cmp_ge_f32 vcc, v151, v165
	v_addc_co_u32 v160, vcc, v160, v160, vcc
	v_cmp_ge_f32 vcc, v151, v164
	v_addc_co_u32 v5, vcc, v5, v5, vcc
	v_cmp_ge_f32 vcc, v150, v165
	v_addc_co_u32 v160, vcc, v160, v160, vcc
	v_cmp_ge_f32 vcc, v150, v164
	v_addc_co_u32 v5, vcc, v5, v5, vcc
	v_cmp_ge_f32 vcc, v149, v165
	v_addc_co_u32 v160, vcc, v160, v160, vcc
	v_cmp_ge_f32 vcc, v149, v164
	v_addc_co_u32 v5, vcc, v5, v5, vcc
	v_cmp_ge_f32 vcc, v148, v165
	v_addc_co_u32 v160, vcc, v160, v160, vcc
	v_cmp_ge_f32 vcc, v148, v164
	v_addc_co_u32 v5, vcc, v5, v5, vcc
	s_nop 0
	v_cmp_ge_f32 vcc, v147, v165
	v_addc_co_u32 v160, vcc, v160, v160, vcc
	s_nop 0
	v_cmp_ge_f32 vcc, v147, v164
	v_addc_co_u32 v5, vcc, v5, v5, vcc
	s_nop 0
	v_cmp_ge_f32 vcc, v146, v165
	v_addc_co_u32 v160, vcc, v160, v160, vcc
	s_nop 0
	v_cmp_ge_f32 vcc, v146, v164
	v_addc_co_u32 v5, vcc, v5, v5, vcc
	s_nop 0
	v_cmp_ge_f32 vcc, v145, v165
	v_addc_co_u32 v160, vcc, v160, v160, vcc
	s_nop 0
	v_cmp_ge_f32 vcc, v145, v164
	v_addc_co_u32 v5, vcc, v5, v5, vcc
	s_nop 0
	v_cmp_ge_f32 vcc, v144, v165
	v_addc_co_u32 v160, vcc, v160, v160, vcc
	s_nop 0
	v_cmp_ge_f32 vcc, v144, v164
	v_addc_co_u32 v5, vcc, v5, v5, vcc
	s_nop 0
	v_bitop3_b32 v3, v5, v160, v5 bitop3:0x30
	v_bitop3_b32 v5, v5, 15, v160 bitop3:0x40
	v_lshlrev_b32_e32 v7, 4, v3
	v_and_or_b32 v5, v7, s93, v5
	v_lshlrev_b32_e32 v7, 8, v3
	v_lshlrev_b32_e32 v9, 12, v3
	v_and_b32_e32 v7, 0xf0000, v7
	v_and_b32_e32 v9, 0xf000000, v9
	v_or3_b32 v143, v5, v7, v9
	v_cmp_ne_u32_e32 vcc, 0, v143
	s_and_b64 s[0:1], s[10:11], vcc
	s_and_saveexec_b64 s[20:21], s[0:1]
	s_cbranch_execz .LBB0_1128
	v_bcnt_u32_b32 v5, v143, 0
	ds_add_rtn_u32 v161, v221, v5
	v_and_b32_e32 v5, 1, v3
	v_cmp_eq_u32_e32 vcc, 1, v5
	s_and_saveexec_b64 s[14:15], vcc
	s_cbranch_execz .LBB0_1070
	s_waitcnt lgkmcnt(0)
	v_cmp_gt_u32_e32 vcc, s87, v161
	s_and_saveexec_b64 s[42:43], vcc
	v_add_f32_e32 v0, 0, v144
	v_ashrrev_i32_e32 v252, 31, v0
	v_bitop3_b32 v0, v252, v0, s85 bitop3:0x36
	v_lshlrev_b64 v[162:163], 16, v[0:1]
	v_add_u32_e32 v0, s45, v142
	v_lshl_add_u32 v5, v161, 3, v136
	v_or_b32_e32 v162, v162, v0
	ds_write_b64 v5, v[162:163] offset:512
	s_or_b64 exec, exec, s[42:43]
	v_add_u32_e32 v161, 1, v161
.LBB0_1070:
	s_or_b64 exec, exec, s[14:15]
	v_and_b32_e32 v0, 2, v3
	v_cmp_ne_u32_e32 vcc, 0, v0
	s_and_saveexec_b64 s[14:15], vcc
	s_cbranch_execz .LBB0_1074
	s_waitcnt lgkmcnt(0)
	v_cmp_gt_u32_e32 vcc, s87, v161
	s_and_saveexec_b64 s[42:43], vcc
	s_cbranch_execz .LBB0_1073
	v_mov_b32_e32 v65, v1
	v_add_f32_e32 v64, 0, v145
	v_ashrrev_i32_e32 v252, 31, v64
	v_bitop3_b32 v64, v252, v64, s85 bitop3:0x36
	v_lshlrev_b64 v[64:65], 16, v[64:65]
	v_add3_u32 v0, s45, v142, -1
	v_or_b32_e32 v64, v64, v0
	v_lshl_add_u32 v0, v161, 3, v136
	ds_write_b64 v0, v[64:65] offset:512

; #define LAS __attribute__((address_space(3)))
; __device__ __forceinline__ int crow(int r, int hi) { return (r & 3) + 8 * (r >> 2) + 4 * hi; }
; __device__ __forceinline__ unsigned fkey2(float v) { const unsigned u = __float_as_uint(v + 0.0f); return u ^ ((unsigned)((int)u >> 31) | 0x80000000u); }
; template <int PASS, bool DIAG> __device__ __forceinline__ void idx_half(unsigned& bits, unsigned& ebits, const f32x16& sc, int sbase, int tq, int r32, int hi, unsigned khi, unsigned klo, bool cand, LAS unsigned char* L) {
;     ...
;             for (int r = 0; r < 16; ++r) if ((ebits >> crow(r, 0)) & 1u) { const int s = sbase + crow(r, hi);
;                 if (slot < (unsigned)IDX_CAP) ((LAS unsigned long long*)(L + IL_CAND))[r32 * IDX_CAP + slot] = ((unsigned long long)fkey2(sc[r]) << 16) | (unsigned long long)(0xFFFFu - (unsigned)s);
.LBB0_1074:
	s_or_b64 exec, exec, s[14:15]
	v_and_b32_e32 v0, 4, v3
	v_cmp_ne_u32_e32 vcc, 0, v0
	s_and_saveexec_b64 s[14:15], vcc
	s_cbranch_execz .LBB0_1078
	s_waitcnt lgkmcnt(0)
	v_cmp_gt_u32_e32 vcc, s87, v161
	s_and_saveexec_b64 s[42:43], vcc
	s_cbranch_execz .LBB0_1077
	v_mov_b32_e32 v63, v1
	v_add_u32_e32 v0, s45, v140
	v_add_f32_e32 v62, 0, v146
	v_ashrrev_i32_e32 v252, 31, v62
	v_bitop3_b32 v62, v252, v62, s85 bitop3:0x36
	v_lshlrev_b64 v[62:63], 16, v[62:63]
	v_add_u32_e32 v0, 0xfffd, v0
	v_or_b32_e32 v62, v62, v0
	v_lshl_add_u32 v0, v161, 3, v136
	ds_write_b64 v0, v[62:63] offset:512

; #define LAS __attribute__((address_space(3)))
; __device__ __forceinline__ int crow(int r, int hi) { return (r & 3) + 8 * (r >> 2) + 4 * hi; }
; __device__ __forceinline__ unsigned fkey2(float v) { const unsigned u = __float_as_uint(v + 0.0f); return u ^ ((unsigned)((int)u >> 31) | 0x80000000u); }
; template <int PASS, bool DIAG> __device__ __forceinline__ void idx_half(unsigned& bits, unsigned& ebits, const f32x16& sc, int sbase, int tq, int r32, int hi, unsigned khi, unsigned klo, bool cand, LAS unsigned char* L) {
;     ...
;             for (int r = 0; r < 16; ++r) if ((ebits >> crow(r, 0)) & 1u) { const int s = sbase + crow(r, hi);
;                 if (slot < (unsigned)IDX_CAP) ((LAS unsigned long long*)(L + IL_CAND))[r32 * IDX_CAP + slot] = ((unsigned long long)fkey2(sc[r]) << 16) | (unsigned long long)(0xFFFFu - (unsigned)s);
.LBB0_1078:
	s_or_b64 exec, exec, s[14:15]
	v_and_b32_e32 v0, 8, v3
	v_cmp_ne_u32_e32 vcc, 0, v0
	s_and_saveexec_b64 s[14:15], vcc
	s_cbranch_execz .LBB0_1082
	s_waitcnt lgkmcnt(0)
	v_cmp_gt_u32_e32 vcc, s87, v161
	s_and_saveexec_b64 s[42:43], vcc
	s_cbranch_execz .LBB0_1081
	v_mov_b32_e32 v61, v1
	v_add_u32_e32 v0, s45, v140
	v_add_f32_e32 v60, 0, v147
	v_ashrrev_i32_e32 v252, 31, v60
	v_bitop3_b32 v60, v252, v60, s85 bitop3:0x36
	v_lshlrev_b64 v[60:61], 16, v[60:61]
	v_add_u32_e32 v0, 0xfffc, v0
	v_or_b32_e32 v60, v60, v0
	v_lshl_add_u32 v0, v161, 3, v136
	ds_write_b64 v0, v[60:61] offset:512

; #define LAS __attribute__((address_space(3)))
; __device__ __forceinline__ int crow(int r, int hi) { return (r & 3) + 8 * (r >> 2) + 4 * hi; }
; __device__ __forceinline__ unsigned fkey2(float v) { const unsigned u = __float_as_uint(v + 0.0f); return u ^ ((unsigned)((int)u >> 31) | 0x80000000u); }
; template <int PASS, bool DIAG> __device__ __forceinline__ void idx_half(unsigned& bits, unsigned& ebits, const f32x16& sc, int sbase, int tq, int r32, int hi, unsigned khi, unsigned klo, bool cand, LAS unsigned char* L) {
;     ...
;             for (int r = 0; r < 16; ++r) if ((ebits >> crow(r, 0)) & 1u) { const int s = sbase + crow(r, hi);
;                 if (slot < (unsigned)IDX_CAP) ((LAS unsigned long long*)(L + IL_CAND))[r32 * IDX_CAP + slot] = ((unsigned long long)fkey2(sc[r]) << 16) | (unsigned long long)(0xFFFFu - (unsigned)s);
.LBB0_1082:
	s_or_b64 exec, exec, s[14:15]
	v_and_b32_e32 v0, 16, v3
	v_cmp_ne_u32_e32 vcc, 0, v0
	s_and_saveexec_b64 s[14:15], vcc
	s_cbranch_execz .LBB0_1086
	s_waitcnt lgkmcnt(0)
	v_cmp_gt_u32_e32 vcc, s87, v161
	s_and_saveexec_b64 s[42:43], vcc
	s_cbranch_execz .LBB0_1085
	v_mov_b32_e32 v59, v1
	v_add_u32_e32 v0, s45, v140
	v_add_f32_e32 v58, 0, v148
	v_ashrrev_i32_e32 v252, 31, v58
	v_bitop3_b32 v58, v252, v58, s85 bitop3:0x36
	v_lshlrev_b64 v[58:59], 16, v[58:59]
	v_add_u32_e32 v0, 0xfff7, v0
	v_or_b32_e32 v58, v58, v0
	v_lshl_add_u32 v0, v161, 3, v136
	ds_write_b64 v0, v[58:59] offset:512

; #define LAS __attribute__((address_space(3)))
; __device__ __forceinline__ int crow(int r, int hi) { return (r & 3) + 8 * (r >> 2) + 4 * hi; }
; __device__ __forceinline__ unsigned fkey2(float v) { const unsigned u = __float_as_uint(v + 0.0f); return u ^ ((unsigned)((int)u >> 31) | 0x80000000u); }
; template <int PASS, bool DIAG> __device__ __forceinline__ void idx_half(unsigned& bits, unsigned& ebits, const f32x16& sc, int sbase, int tq, int r32, int hi, unsigned khi, unsigned klo, bool cand, LAS unsigned char* L) {
;     ...
;             for (int r = 0; r < 16; ++r) if ((ebits >> crow(r, 0)) & 1u) { const int s = sbase + crow(r, hi);
;                 if (slot < (unsigned)IDX_CAP) ((LAS unsigned long long*)(L + IL_CAND))[r32 * IDX_CAP + slot] = ((unsigned long long)fkey2(sc[r]) << 16) | (unsigned long long)(0xFFFFu - (unsigned)s);
.LBB0_1086:
	s_or_b64 exec, exec, s[14:15]
	v_and_b32_e32 v0, 32, v3
	v_cmp_ne_u32_e32 vcc, 0, v0
	s_and_saveexec_b64 s[14:15], vcc
	s_cbranch_execz .LBB0_1090
	s_waitcnt lgkmcnt(0)
	v_cmp_gt_u32_e32 vcc, s87, v161
	s_and_saveexec_b64 s[42:43], vcc
	s_cbranch_execz .LBB0_1089
	v_mov_b32_e32 v57, v1
	v_add_u32_e32 v0, s45, v140
	v_add_f32_e32 v56, 0, v149
	v_ashrrev_i32_e32 v252, 31, v56
	v_bitop3_b32 v56, v252, v56, s85 bitop3:0x36
	v_lshlrev_b64 v[56:57], 16, v[56:57]
	v_add_u32_e32 v0, 0xfff6, v0
	v_or_b32_e32 v56, v56, v0
	v_lshl_add_u32 v0, v161, 3, v136
	ds_write_b64 v0, v[56:57] offset:512

; #define LAS __attribute__((address_space(3)))
; __device__ __forceinline__ int crow(int r, int hi) { return (r & 3) + 8 * (r >> 2) + 4 * hi; }
; __device__ __forceinline__ unsigned fkey2(float v) { const unsigned u = __float_as_uint(v + 0.0f); return u ^ ((unsigned)((int)u >> 31) | 0x80000000u); }
; template <int PASS, bool DIAG> __device__ __forceinline__ void idx_half(unsigned& bits, unsigned& ebits, const f32x16& sc, int sbase, int tq, int r32, int hi, unsigned khi, unsigned klo, bool cand, LAS unsigned char* L) {
;     ...
;             for (int r = 0; r < 16; ++r) if ((ebits >> crow(r, 0)) & 1u) { const int s = sbase + crow(r, hi);
;                 if (slot < (unsigned)IDX_CAP) ((LAS unsigned long long*)(L + IL_CAND))[r32 * IDX_CAP + slot] = ((unsigned long long)fkey2(sc[r]) << 16) | (unsigned long long)(0xFFFFu - (unsigned)s);
.LBB0_1090:
	s_or_b64 exec, exec, s[14:15]
	v_and_b32_e32 v0, 64, v3
	v_cmp_ne_u32_e32 vcc, 0, v0
	s_and_saveexec_b64 s[14:15], vcc
	s_cbranch_execz .LBB0_1094
	s_waitcnt lgkmcnt(0)
	v_cmp_gt_u32_e32 vcc, s87, v161
	s_and_saveexec_b64 s[42:43], vcc
	s_cbranch_execz .LBB0_1093
	v_mov_b32_e32 v55, v1
	v_add_u32_e32 v0, s45, v140
	v_add_f32_e32 v54, 0, v150
	v_ashrrev_i32_e32 v252, 31, v54
	v_bitop3_b32 v54, v252, v54, s85 bitop3:0x36
	v_lshlrev_b64 v[54:55], 16, v[54:55]
	v_add_u32_e32 v0, 0xfff5, v0
	v_or_b32_e32 v54, v54, v0
	v_lshl_add_u32 v0, v161, 3, v136
	ds_write_b64 v0, v[54:55] offset:512

; #define LAS __attribute__((address_space(3)))
; __device__ __forceinline__ int crow(int r, int hi) { return (r & 3) + 8 * (r >> 2) + 4 * hi; }
; __device__ __forceinline__ unsigned fkey2(float v) { const unsigned u = __float_as_uint(v + 0.0f); return u ^ ((unsigned)((int)u >> 31) | 0x80000000u); }
; template <int PASS, bool DIAG> __device__ __forceinline__ void idx_half(unsigned& bits, unsigned& ebits, const f32x16& sc, int sbase, int tq, int r32, int hi, unsigned khi, unsigned klo, bool cand, LAS unsigned char* L) {
;     ...
;             for (int r = 0; r < 16; ++r) if ((ebits >> crow(r, 0)) & 1u) { const int s = sbase + crow(r, hi);
;                 if (slot < (unsigned)IDX_CAP) ((LAS unsigned long long*)(L + IL_CAND))[r32 * IDX_CAP + slot] = ((unsigned long long)fkey2(sc[r]) << 16) | (unsigned long long)(0xFFFFu - (unsigned)s);
.LBB0_1094:
	s_or_b64 exec, exec, s[14:15]
	v_and_b32_e32 v0, 0x80, v3
	v_cmp_ne_u32_e32 vcc, 0, v0
	s_and_saveexec_b64 s[14:15], vcc
	s_cbranch_execz .LBB0_1098
	s_waitcnt lgkmcnt(0)
	v_cmp_gt_u32_e32 vcc, s87, v161
	s_and_saveexec_b64 s[42:43], vcc
	s_cbranch_execz .LBB0_1097
	v_mov_b32_e32 v53, v1
	v_add_u32_e32 v0, s45, v140
	v_add_f32_e32 v52, 0, v151
	v_ashrrev_i32_e32 v252, 31, v52
	v_bitop3_b32 v52, v252, v52, s85 bitop3:0x36
	v_lshlrev_b64 v[52:53], 16, v[52:53]
	v_add_u32_e32 v0, 0xfff4, v0
	v_or_b32_e32 v52, v52, v0
	v_lshl_add_u32 v0, v161, 3, v136
	ds_write_b64 v0, v[52:53] offset:512

; #define LAS __attribute__((address_space(3)))
; __device__ __forceinline__ int crow(int r, int hi) { return (r & 3) + 8 * (r >> 2) + 4 * hi; }
; __device__ __forceinline__ unsigned fkey2(float v) { const unsigned u = __float_as_uint(v + 0.0f); return u ^ ((unsigned)((int)u >> 31) | 0x80000000u); }
; template <int PASS, bool DIAG> __device__ __forceinline__ void idx_half(unsigned& bits, unsigned& ebits, const f32x16& sc, int sbase, int tq, int r32, int hi, unsigned khi, unsigned klo, bool cand, LAS unsigned char* L) {
;     ...
;             for (int r = 0; r < 16; ++r) if ((ebits >> crow(r, 0)) & 1u) { const int s = sbase + crow(r, hi);
;                 if (slot < (unsigned)IDX_CAP) ((LAS unsigned long long*)(L + IL_CAND))[r32 * IDX_CAP + slot] = ((unsigned long long)fkey2(sc[r]) << 16) | (unsigned long long)(0xFFFFu - (unsigned)s);
.LBB0_1098:
	s_or_b64 exec, exec, s[14:15]
	v_and_b32_e32 v0, 0x100, v3
	v_cmp_ne_u32_e32 vcc, 0, v0
	s_and_saveexec_b64 s[14:15], vcc
	s_cbranch_execz .LBB0_1102
	s_waitcnt lgkmcnt(0)
	v_cmp_gt_u32_e32 vcc, s87, v161
	s_and_saveexec_b64 s[42:43], vcc
	s_cbranch_execz .LBB0_1101
	v_mov_b32_e32 v17, v1
	v_add_u32_e32 v0, s45, v140
	v_add_f32_e32 v16, 0, v152
	v_ashrrev_i32_e32 v252, 31, v16
	v_bitop3_b32 v16, v252, v16, s85 bitop3:0x36
	v_lshlrev_b64 v[16:17], 16, v[16:17]
	v_add_u32_e32 v0, 0xffef, v0
	v_or_b32_e32 v16, v16, v0
	v_lshl_add_u32 v0, v161, 3, v136
	ds_write_b64 v0, v[16:17] offset:512

; #define LAS __attribute__((address_space(3)))
; __device__ __forceinline__ int crow(int r, int hi) { return (r & 3) + 8 * (r >> 2) + 4 * hi; }
; __device__ __forceinline__ unsigned fkey2(float v) { const unsigned u = __float_as_uint(v + 0.0f); return u ^ ((unsigned)((int)u >> 31) | 0x80000000u); }
; template <int PASS, bool DIAG> __device__ __forceinline__ void idx_half(unsigned& bits, unsigned& ebits, const f32x16& sc, int sbase, int tq, int r32, int hi, unsigned khi, unsigned klo, bool cand, LAS unsigned char* L) {
;     ...
;             for (int r = 0; r < 16; ++r) if ((ebits >> crow(r, 0)) & 1u) { const int s = sbase + crow(r, hi);
;                 if (slot < (unsigned)IDX_CAP) ((LAS unsigned long long*)(L + IL_CAND))[r32 * IDX_CAP + slot] = ((unsigned long long)fkey2(sc[r]) << 16) | (unsigned long long)(0xFFFFu - (unsigned)s);
.LBB0_1102:
	s_or_b64 exec, exec, s[14:15]
	v_and_b32_e32 v0, 0x200, v3
	v_cmp_ne_u32_e32 vcc, 0, v0
	s_and_saveexec_b64 s[14:15], vcc
	s_cbranch_execz .LBB0_1106
	s_waitcnt lgkmcnt(0)
	v_cmp_gt_u32_e32 vcc, s87, v161
	s_and_saveexec_b64 s[42:43], vcc
	s_cbranch_execz .LBB0_1105
	v_mov_b32_e32 v15, v1
	v_add_u32_e32 v0, s45, v140
	v_add_f32_e32 v14, 0, v153
	v_ashrrev_i32_e32 v252, 31, v14
	v_bitop3_b32 v14, v252, v14, s85 bitop3:0x36
	v_lshlrev_b64 v[14:15], 16, v[14:15]
	v_add_u32_e32 v0, 0xffee, v0
	v_or_b32_e32 v14, v14, v0
	v_lshl_add_u32 v0, v161, 3, v136
	ds_write_b64 v0, v[14:15] offset:512

; #define LAS __attribute__((address_space(3)))
; __device__ __forceinline__ int crow(int r, int hi) { return (r & 3) + 8 * (r >> 2) + 4 * hi; }
; __device__ __forceinline__ unsigned fkey2(float v) { const unsigned u = __float_as_uint(v + 0.0f); return u ^ ((unsigned)((int)u >> 31) | 0x80000000u); }
; template <int PASS, bool DIAG> __device__ __forceinline__ void idx_half(unsigned& bits, unsigned& ebits, const f32x16& sc, int sbase, int tq, int r32, int hi, unsigned khi, unsigned klo, bool cand, LAS unsigned char* L) {
;     ...
;             for (int r = 0; r < 16; ++r) if ((ebits >> crow(r, 0)) & 1u) { const int s = sbase + crow(r, hi);
;                 if (slot < (unsigned)IDX_CAP) ((LAS unsigned long long*)(L + IL_CAND))[r32 * IDX_CAP + slot] = ((unsigned long long)fkey2(sc[r]) << 16) | (unsigned long long)(0xFFFFu - (unsigned)s);
.LBB0_1106:
	s_or_b64 exec, exec, s[14:15]
	v_and_b32_e32 v0, 0x400, v3
	v_cmp_ne_u32_e32 vcc, 0, v0
	s_and_saveexec_b64 s[14:15], vcc
	s_cbranch_execz .LBB0_1110
	s_waitcnt lgkmcnt(0)
	v_cmp_gt_u32_e32 vcc, s87, v161
	s_and_saveexec_b64 s[42:43], vcc
	s_cbranch_execz .LBB0_1109
	v_mov_b32_e32 v13, v1
	v_add_u32_e32 v0, s45, v140
	v_add_f32_e32 v12, 0, v154
	v_ashrrev_i32_e32 v252, 31, v12
	v_bitop3_b32 v12, v252, v12, s85 bitop3:0x36
	v_lshlrev_b64 v[12:13], 16, v[12:13]
	v_add_u32_e32 v0, 0xffed, v0
	v_or_b32_e32 v12, v12, v0
	v_lshl_add_u32 v0, v161, 3, v136
	ds_write_b64 v0, v[12:13] offset:512

; #define LAS __attribute__((address_space(3)))
; __device__ __forceinline__ int crow(int r, int hi) { return (r & 3) + 8 * (r >> 2) + 4 * hi; }
; __device__ __forceinline__ unsigned fkey2(float v) { const unsigned u = __float_as_uint(v + 0.0f); return u ^ ((unsigned)((int)u >> 31) | 0x80000000u); }
; template <int PASS, bool DIAG> __device__ __forceinline__ void idx_half(unsigned& bits, unsigned& ebits, const f32x16& sc, int sbase, int tq, int r32, int hi, unsigned khi, unsigned klo, bool cand, LAS unsigned char* L) {
;     ...
;             for (int r = 0; r < 16; ++r) if ((ebits >> crow(r, 0)) & 1u) { const int s = sbase + crow(r, hi);
;                 if (slot < (unsigned)IDX_CAP) ((LAS unsigned long long*)(L + IL_CAND))[r32 * IDX_CAP + slot] = ((unsigned long long)fkey2(sc[r]) << 16) | (unsigned long long)(0xFFFFu - (unsigned)s);
.LBB0_1110:
	s_or_b64 exec, exec, s[14:15]
	v_and_b32_e32 v0, 0x800, v3
	v_cmp_ne_u32_e32 vcc, 0, v0
	s_and_saveexec_b64 s[14:15], vcc
	s_cbranch_execz .LBB0_1114
	s_waitcnt lgkmcnt(0)
	v_cmp_gt_u32_e32 vcc, s87, v161
	s_and_saveexec_b64 s[42:43], vcc
	s_cbranch_execz .LBB0_1113
	v_mov_b32_e32 v11, v1
	v_add_u32_e32 v0, s45, v140
	v_add_f32_e32 v10, 0, v155
	v_ashrrev_i32_e32 v252, 31, v10
	v_bitop3_b32 v10, v252, v10, s85 bitop3:0x36
	v_lshlrev_b64 v[10:11], 16, v[10:11]
	v_add_u32_e32 v0, 0xffec, v0
	v_or_b32_e32 v10, v10, v0
	v_lshl_add_u32 v0, v161, 3, v136
	ds_write_b64 v0, v[10:11] offset:512

; #define LAS __attribute__((address_space(3)))
; __device__ __forceinline__ int crow(int r, int hi) { return (r & 3) + 8 * (r >> 2) + 4 * hi; }
; __device__ __forceinline__ unsigned fkey2(float v) { const unsigned u = __float_as_uint(v + 0.0f); return u ^ ((unsigned)((int)u >> 31) | 0x80000000u); }
; template <int PASS, bool DIAG> __device__ __forceinline__ void idx_half(unsigned& bits, unsigned& ebits, const f32x16& sc, int sbase, int tq, int r32, int hi, unsigned khi, unsigned klo, bool cand, LAS unsigned char* L) {
;     ...
;             for (int r = 0; r < 16; ++r) if ((ebits >> crow(r, 0)) & 1u) { const int s = sbase + crow(r, hi);
;                 if (slot < (unsigned)IDX_CAP) ((LAS unsigned long long*)(L + IL_CAND))[r32 * IDX_CAP + slot] = ((unsigned long long)fkey2(sc[r]) << 16) | (unsigned long long)(0xFFFFu - (unsigned)s);
.LBB0_1114:
	s_or_b64 exec, exec, s[14:15]
	v_and_b32_e32 v0, 0x1000, v3
	v_cmp_ne_u32_e32 vcc, 0, v0
	s_and_saveexec_b64 s[14:15], vcc
	s_cbranch_execz .LBB0_1118
	s_waitcnt lgkmcnt(0)
	v_cmp_gt_u32_e32 vcc, s87, v161
	s_and_saveexec_b64 s[42:43], vcc
	s_cbranch_execz .LBB0_1117
	v_mov_b32_e32 v9, v1
	v_add_u32_e32 v0, s45, v140
	v_add_f32_e32 v8, 0, v156
	v_ashrrev_i32_e32 v252, 31, v8
	v_bitop3_b32 v8, v252, v8, s85 bitop3:0x36
	v_lshlrev_b64 v[8:9], 16, v[8:9]
	v_add_u32_e32 v0, 0xffe7, v0
	v_or_b32_e32 v8, v8, v0
	v_lshl_add_u32 v0, v161, 3, v136
	ds_write_b64 v0, v[8:9] offset:512

; #define LAS __attribute__((address_space(3)))
; __device__ __forceinline__ int crow(int r, int hi) { return (r & 3) + 8 * (r >> 2) + 4 * hi; }
; __device__ __forceinline__ unsigned fkey2(float v) { const unsigned u = __float_as_uint(v + 0.0f); return u ^ ((unsigned)((int)u >> 31) | 0x80000000u); }
; template <int PASS, bool DIAG> __device__ __forceinline__ void idx_half(unsigned& bits, unsigned& ebits, const f32x16& sc, int sbase, int tq, int r32, int hi, unsigned khi, unsigned klo, bool cand, LAS unsigned char* L) {
;     ...
;             for (int r = 0; r < 16; ++r) if ((ebits >> crow(r, 0)) & 1u) { const int s = sbase + crow(r, hi);
;                 if (slot < (unsigned)IDX_CAP) ((LAS unsigned long long*)(L + IL_CAND))[r32 * IDX_CAP + slot] = ((unsigned long long)fkey2(sc[r]) << 16) | (unsigned long long)(0xFFFFu - (unsigned)s);
.LBB0_1118:
	s_or_b64 exec, exec, s[14:15]
	v_and_b32_e32 v0, 0x2000, v3
	v_cmp_ne_u32_e32 vcc, 0, v0
	s_and_saveexec_b64 s[14:15], vcc
	s_cbranch_execz .LBB0_1122
	s_waitcnt lgkmcnt(0)
	v_cmp_gt_u32_e32 vcc, s87, v161
	s_and_saveexec_b64 s[42:43], vcc
	s_cbranch_execz .LBB0_1121
	v_mov_b32_e32 v7, v1
	v_add_u32_e32 v0, s45, v140
	v_add_f32_e32 v6, 0, v157
	v_ashrrev_i32_e32 v252, 31, v6
	v_bitop3_b32 v6, v252, v6, s85 bitop3:0x36
	v_lshlrev_b64 v[6:7], 16, v[6:7]
	v_add_u32_e32 v0, 0xffe6, v0
	v_or_b32_e32 v6, v6, v0
	v_lshl_add_u32 v0, v161, 3, v136
	ds_write_b64 v0, v[6:7] offset:512

; #define LAS __attribute__((address_space(3)))
; __device__ __forceinline__ int crow(int r, int hi) { return (r & 3) + 8 * (r >> 2) + 4 * hi; }
; __device__ __forceinline__ unsigned fkey2(float v) { const unsigned u = __float_as_uint(v + 0.0f); return u ^ ((unsigned)((int)u >> 31) | 0x80000000u); }
; template <int PASS, bool DIAG> __device__ __forceinline__ void idx_half(unsigned& bits, unsigned& ebits, const f32x16& sc, int sbase, int tq, int r32, int hi, unsigned khi, unsigned klo, bool cand, LAS unsigned char* L) {
;     ...
;             for (int r = 0; r < 16; ++r) if ((ebits >> crow(r, 0)) & 1u) { const int s = sbase + crow(r, hi);
;                 if (slot < (unsigned)IDX_CAP) ((LAS unsigned long long*)(L + IL_CAND))[r32 * IDX_CAP + slot] = ((unsigned long long)fkey2(sc[r]) << 16) | (unsigned long long)(0xFFFFu - (unsigned)s);
.LBB0_1122:
	s_or_b64 exec, exec, s[14:15]
	v_and_b32_e32 v0, 0x4000, v3
	v_cmp_ne_u32_e32 vcc, 0, v0
	s_and_saveexec_b64 s[14:15], vcc
	s_cbranch_execz .LBB0_1126
	s_waitcnt lgkmcnt(0)
	v_cmp_gt_u32_e32 vcc, s87, v161
	s_and_saveexec_b64 s[42:43], vcc
	s_cbranch_execz .LBB0_1125
	v_mov_b32_e32 v5, v1
	v_add_u32_e32 v0, s45, v140
	v_add_f32_e32 v4, 0, v158
	v_ashrrev_i32_e32 v252, 31, v4
	v_bitop3_b32 v4, v252, v4, s85 bitop3:0x36
	v_lshlrev_b64 v[4:5], 16, v[4:5]
	v_add_u32_e32 v0, 0xffe5, v0
	v_or_b32_e32 v4, v4, v0
	v_lshl_add_u32 v0, v161, 3, v136
	ds_write_b64 v0, v[4:5] offset:512

; #define LAS __attribute__((address_space(3)))
; __device__ __forceinline__ int crow(int r, int hi) { return (r & 3) + 8 * (r >> 2) + 4 * hi; }
; __device__ __forceinline__ unsigned fkey2(float v) { const unsigned u = __float_as_uint(v + 0.0f); return u ^ ((unsigned)((int)u >> 31) | 0x80000000u); }
; template <int PASS, bool DIAG> __device__ __forceinline__ void idx_half(unsigned& bits, unsigned& ebits, const f32x16& sc, int sbase, int tq, int r32, int hi, unsigned khi, unsigned klo, bool cand, LAS unsigned char* L) {
;     ...
;             for (int r = 0; r < 16; ++r) if ((ebits >> crow(r, 0)) & 1u) { const int s = sbase + crow(r, hi);
;                 if (slot < (unsigned)IDX_CAP) ((LAS unsigned long long*)(L + IL_CAND))[r32 * IDX_CAP + slot] = ((unsigned long long)fkey2(sc[r]) << 16) | (unsigned long long)(0xFFFFu - (unsigned)s);
.LBB0_1126:
	s_or_b64 exec, exec, s[14:15]
	v_and_b32_e32 v0, 0x8000, v3
	v_cmp_ne_u32_e32 vcc, 0, v0
	s_waitcnt lgkmcnt(0)
	v_cmp_gt_u32_e64 s[14:15], s87, v161
	s_and_b64 s[0:1], vcc, s[14:15]
	s_and_b64 exec, exec, s[0:1]
	s_cbranch_execz .LBB0_1128
	v_mov_b32_e32 v3, v1
	v_add_u32_e32 v0, s45, v140
	v_add_f32_e32 v2, 0, v159
	v_ashrrev_i32_e32 v252, 31, v2
	v_bitop3_b32 v2, v252, v2, s85 bitop3:0x36
	v_lshlrev_b64 v[2:3], 16, v[2:3]
	v_add_u32_e32 v0, 0xffe4, v0
	v_or_b32_e32 v2, v2, v0
	v_lshl_add_u32 v0, v161, 3, v136
	ds_write_b64 v0, v[2:3] offset:512

; __device__ __forceinline__ float relu_i(float p) { const int i = __float_as_int(p); return __int_as_float(i > 0 ? i : 0); }
; __device__ __forceinline__ void idx_scores_k(f32x16& sc, const bf16x8 (&kf)[4], const bf16x8 (&qf)[16], const f32x4& w) {
;     f32x16 p0 = f32x16{}, p1 = f32x16{};
; #pragma unroll
;     for (int d0 = 0; d0 < 4; ++d0) p0 = __builtin_amdgcn_mfma_f32_32x32x16_bf16(kf[d0], qf[d0], p0, 0, 0, 0);
; #pragma unroll
;     for (int d0 = 0; d0 < 4; ++d0) p1 = __builtin_amdgcn_mfma_f32_32x32x16_bf16(kf[d0], qf[4 + d0], p1, 0, 0, 0);
; #pragma unroll
;     for (int r = 0; r < 16; ++r) sc[r] = w[0] * relu_i(p0[r]);
;     p0 = f32x16{};
; #pragma unroll
;     for (int d0 = 0; d0 < 4; ++d0) p0 = __builtin_amdgcn_mfma_f32_32x32x16_bf16(kf[d0], qf[8 + d0], p0, 0, 0, 0);
; #pragma unroll
;     for (int r = 0; r < 16; ++r) sc[r] = fmaf(w[1], relu_i(p1[r]), sc[r]);
;     p1 = f32x16{};
; #pragma unroll
;     for (int d0 = 0; d0 < 4; ++d0) p1 = __builtin_amdgcn_mfma_f32_32x32x16_bf16(kf[d0], qf[12 + d0], p1, 0, 0, 0);
; #pragma unroll
;     for (int r = 0; r < 16; ++r) sc[r] = fmaf(w[2], relu_i(p0[r]), sc[r]);
; #pragma unroll
;     for (int r = 0; r < 16; ++r) sc[r] = fmaf(w[3], relu_i(p1[r]), sc[r]);
; }
; template <int PASS> __device__ __forceinline__ void idx_pass(const bf16_t* KIb, const bf16x8 (&qf)[16], const f32x4& w, int jd, int tq, int wid, int r32, int hi, unsigned khi, unsigned klo, bool cand, LAS unsigned char* L) {
;     ...
;         idx_scores_k(sc, kB, qf, w);
;         if (diag) idx_half<PASS, true>(hw, ehw, sc, j * 64 + 32, tq, r32, hi, khi, klo, cand, L); else idx_half<PASS, false>(hw, ehw, sc, j * 64 + 32, tq, r32, hi, khi, klo, cand, L);
.LBB0_1131:
	s_mov_b64 s[14:15], -1
	s_and_b64 vcc, exec, s[18:19]
	s_waitcnt vmcnt(3)
	v_mfma_f32_32x32x16_bf16 v[2:17], v[46:49], v[70:73], 0
	s_waitcnt vmcnt(2)
	v_mfma_f32_32x32x16_bf16 v[2:17], v[42:45], v[74:77], v[2:17]
	s_waitcnt vmcnt(1)
	v_mfma_f32_32x32x16_bf16 v[2:17], v[38:41], v[78:81], v[2:17]
	s_waitcnt vmcnt(0)
	v_mfma_f32_32x32x16_bf16 v[2:17], v[34:37], v[82:85], v[2:17]
	v_mfma_f32_32x32x16_bf16 v[180:195], v[46:49], v[86:89], 0
	v_mfma_f32_32x32x16_bf16 v[180:195], v[42:45], v[90:93], v[180:195]
	v_mfma_f32_32x32x16_bf16 v[180:195], v[38:41], v[94:97], v[180:195]
	v_mfma_f32_32x32x16_bf16 v[180:195], v[34:37], v[98:101], v[180:195]
	s_nop 7
	v_max_i32_e32 v200, 0, v2
	v_mul_f32_e32 v53, v66, v200
	v_max_i32_e32 v200, 0, v3
	v_mul_f32_e32 v54, v66, v200
	v_max_i32_e32 v200, 0, v4
	v_mul_f32_e32 v55, v66, v200
	v_max_i32_e32 v200, 0, v5
	v_mul_f32_e32 v56, v66, v200
	v_max_i32_e32 v200, 0, v6
	v_mul_f32_e32 v57, v66, v200
	v_max_i32_e32 v200, 0, v7
	v_mul_f32_e32 v58, v66, v200
	v_max_i32_e32 v200, 0, v8
	v_mul_f32_e32 v59, v66, v200
	v_max_i32_e32 v200, 0, v9
	v_mul_f32_e32 v60, v66, v200
	v_max_i32_e32 v200, 0, v10
	v_mul_f32_e32 v61, v66, v200
	v_max_i32_e32 v200, 0, v11
	v_mul_f32_e32 v62, v66, v200
	v_max_i32_e32 v200, 0, v12
	v_mul_f32_e32 v63, v66, v200
	v_max_i32_e32 v200, 0, v13
	v_mul_f32_e32 v64, v66, v200
	v_max_i32_e32 v200, 0, v14
	v_mul_f32_e32 v65, v66, v200
	v_max_i32_e32 v200, 0, v15
	v_mul_f32_e32 v144, v66, v200
	v_max_i32_e32 v200, 0, v16
	v_mul_f32_e32 v145, v66, v200
	v_max_i32_e32 v200, 0, v17
	v_mul_f32_e32 v146, v66, v200
	v_mfma_f32_32x32x16_bf16 v[2:17], v[46:49], v[102:105], 0
	v_mfma_f32_32x32x16_bf16 v[2:17], v[42:45], v[106:109], v[2:17]
	v_mfma_f32_32x32x16_bf16 v[2:17], v[38:41], v[110:113], v[2:17]
	v_mfma_f32_32x32x16_bf16 v[2:17], v[34:37], v[114:117], v[2:17]
	v_max_i32_e32 v200, 0, v180
	v_fmac_f32_e32 v53, v67, v200
	v_max_i32_e32 v200, 0, v181
	v_fmac_f32_e32 v54, v67, v200
	v_max_i32_e32 v200, 0, v182
	v_fmac_f32_e32 v55, v67, v200
	v_max_i32_e32 v200, 0, v183
	v_fmac_f32_e32 v56, v67, v200
	v_max_i32_e32 v200, 0, v184
	v_fmac_f32_e32 v57, v67, v200
	v_max_i32_e32 v200, 0, v185
	v_fmac_f32_e32 v58, v67, v200
	v_max_i32_e32 v200, 0, v186
	v_fmac_f32_e32 v59, v67, v200
	v_max_i32_e32 v200, 0, v187
	v_fmac_f32_e32 v60, v67, v200
	v_max_i32_e32 v200, 0, v188
	v_fmac_f32_e32 v61, v67, v200
	v_max_i32_e32 v200, 0, v189
	v_fmac_f32_e32 v62, v67, v200
	v_max_i32_e32 v200, 0, v190
	v_fmac_f32_e32 v63, v67, v200
	v_max_i32_e32 v200, 0, v191
	v_fmac_f32_e32 v64, v67, v200
	v_max_i32_e32 v200, 0, v192
	v_fmac_f32_e32 v65, v67, v200
	v_max_i32_e32 v200, 0, v193
	v_fmac_f32_e32 v144, v67, v200
	v_max_i32_e32 v200, 0, v194
	v_fmac_f32_e32 v145, v67, v200
	v_max_i32_e32 v200, 0, v195
	v_fmac_f32_e32 v146, v67, v200
	v_mfma_f32_32x32x16_bf16 v[180:195], v[46:49], v[118:121], 0
	v_mfma_f32_32x32x16_bf16 v[180:195], v[42:45], v[122:125], v[180:195]
	v_mfma_f32_32x32x16_bf16 v[180:195], v[38:41], v[126:129], v[180:195]
	v_mfma_f32_32x32x16_bf16 v[180:195], v[34:37], v[130:133], v[180:195]
	v_max_i32_e32 v200, 0, v2
	v_fmac_f32_e32 v53, v68, v200
	v_max_i32_e32 v200, 0, v3
	v_fmac_f32_e32 v54, v68, v200
	v_max_i32_e32 v200, 0, v4
	v_fmac_f32_e32 v55, v68, v200
	v_max_i32_e32 v200, 0, v5
	v_fmac_f32_e32 v56, v68, v200
	v_max_i32_e32 v200, 0, v6
	v_fmac_f32_e32 v57, v68, v200
	v_max_i32_e32 v200, 0, v7
	v_fmac_f32_e32 v58, v68, v200
	v_max_i32_e32 v200, 0, v8
	v_fmac_f32_e32 v59, v68, v200
	v_max_i32_e32 v200, 0, v9
	v_fmac_f32_e32 v60, v68, v200
	v_max_i32_e32 v200, 0, v10
	v_fmac_f32_e32 v61, v68, v200
	v_max_i32_e32 v200, 0, v11
	v_fmac_f32_e32 v62, v68, v200
	v_max_i32_e32 v200, 0, v12
	v_fmac_f32_e32 v63, v68, v200
	v_max_i32_e32 v200, 0, v13
	v_fmac_f32_e32 v64, v68, v200
	v_max_i32_e32 v200, 0, v14
	v_fmac_f32_e32 v65, v68, v200
	v_max_i32_e32 v200, 0, v15
	v_fmac_f32_e32 v144, v68, v200
	v_max_i32_e32 v200, 0, v16
	v_fmac_f32_e32 v145, v68, v200
	v_max_i32_e32 v200, 0, v17
	v_fmac_f32_e32 v146, v68, v200
	v_max_i32_e32 v200, 0, v180
	v_fmac_f32_e32 v53, v69, v200
	v_max_i32_e32 v200, 0, v181
	v_fmac_f32_e32 v54, v69, v200
	v_max_i32_e32 v200, 0, v182
	v_fmac_f32_e32 v55, v69, v200
	v_max_i32_e32 v200, 0, v183
	v_fmac_f32_e32 v56, v69, v200
	v_max_i32_e32 v200, 0, v184
	v_fmac_f32_e32 v57, v69, v200
	v_max_i32_e32 v200, 0, v185
	v_fmac_f32_e32 v58, v69, v200
	v_max_i32_e32 v200, 0, v186
	v_fmac_f32_e32 v59, v69, v200
	v_max_i32_e32 v200, 0, v187
	v_fmac_f32_e32 v60, v69, v200
	v_max_i32_e32 v200, 0, v188
	v_fmac_f32_e32 v61, v69, v200
	v_max_i32_e32 v200, 0, v189
	v_fmac_f32_e32 v62, v69, v200
	v_max_i32_e32 v200, 0, v190
	v_fmac_f32_e32 v63, v69, v200
	v_max_i32_e32 v200, 0, v191
	v_fmac_f32_e32 v64, v69, v200
	v_max_i32_e32 v200, 0, v192
	v_fmac_f32_e32 v65, v69, v200
	v_max_i32_e32 v200, 0, v193
	v_fmac_f32_e32 v144, v69, v200
	v_max_i32_e32 v200, 0, v194
	v_fmac_f32_e32 v145, v69, v200
	v_max_i32_e32 v200, 0, v195
	v_fmac_f32_e32 v146, v69, v200
	s_cbranch_vccz .LBB0_1196
; #define LAS __attribute__((address_space(3)))
; __device__ __forceinline__ int crow(int r, int hi) { return (r & 3) + 8 * (r >> 2) + 4 * hi; }
; __device__ __forceinline__ unsigned fkey2(float v) { const unsigned u = __float_as_uint(v + 0.0f); return u ^ ((unsigned)((int)u >> 31) | 0x80000000u); }
; __device__ __forceinline__ void shl_ge(unsigned& acc, unsigned key, unsigned thr) { asm("v_cmp_ge_u32 vcc, %1, %2\n\tv_addc_co_u32 %0, vcc, %0, %0, vcc" : "+v"(acc) : "v"(key), "v"(thr) : "vcc"); }
; __device__ __forceinline__ unsigned spread4(unsigned x) { return (x & 0xFu) | ((x & 0xF0u) << 4) | ((x & 0xF00u) << 8) | ((x & 0xF000u) << 12); }
; template <int PASS, bool DIAG> __device__ __forceinline__ void idx_half(unsigned& bits, unsigned& ebits, const f32x16& sc, int sbase, int tq, int r32, int hi, unsigned khi, unsigned klo, bool cand, LAS unsigned char* L) {
;     ...
;         unsigned hb = 0u, lb = 0u;
; #pragma unroll
;         for (int r = 15; r >= 0; --r) { const unsigned key = fkey2(sc[r]); shl_ge(hb, key, khi); shl_ge(lb, key, klo); }
;         bits = spread4(hb); ebits = spread4(lb & ~hb);
;         if (DIAG) { const unsigned vm = d < 0 ? 0u : (d >= 31 ? 0xFFFFFFFFu : ((2u << d) - 1u)); bits &= vm; ebits &= vm; }
;         if (cand && ebits != 0u) {
;             unsigned slot = __hip_atomic_fetch_add((LAS unsigned*)(L + IL_CNT) + r32, (unsigned)__builtin_popcount(ebits), __ATOMIC_RELAXED, __HIP_MEMORY_SCOPE_WORKGROUP);
; #pragma unroll
;             for (int r = 0; r < 16; ++r) if ((ebits >> crow(r, 0)) & 1u) { const int s = sbase + crow(r, hi);
;                 if (slot < (unsigned)IDX_CAP) ((LAS unsigned long long*)(L + IL_CAND))[r32 * IDX_CAP + slot] = ((unsigned long long)fkey2(sc[r]) << 16) | (unsigned long long)(0xFFFFu - (unsigned)s);
;                 ++slot; }
	v_mov_b32_e32 v49, 0
	v_mov_b32_e32 v5, 0
	v_cmp_ge_f32 vcc, v146, v165
	v_addc_co_u32 v49, vcc, v49, v49, vcc
	v_cmp_ge_f32 vcc, v146, v164
	v_addc_co_u32 v5, vcc, v5, v5, vcc
	v_cmp_ge_f32 vcc, v145, v165
	v_addc_co_u32 v49, vcc, v49, v49, vcc
	v_cmp_ge_f32 vcc, v145, v164
	v_addc_co_u32 v5, vcc, v5, v5, vcc
	v_cmp_ge_f32 vcc, v144, v165
	v_addc_co_u32 v49, vcc, v49, v49, vcc
	v_cmp_ge_f32 vcc, v144, v164
	v_addc_co_u32 v5, vcc, v5, v5, vcc
	v_cmp_ge_f32 vcc, v65, v165
	v_addc_co_u32 v49, vcc, v49, v49, vcc
	v_cmp_ge_f32 vcc, v65, v164
	v_addc_co_u32 v5, vcc, v5, v5, vcc
	v_cmp_ge_f32 vcc, v64, v165
	v_addc_co_u32 v49, vcc, v49, v49, vcc
	v_cmp_ge_f32 vcc, v64, v164
	v_addc_co_u32 v5, vcc, v5, v5, vcc
	v_cmp_ge_f32 vcc, v63, v165
	v_addc_co_u32 v49, vcc, v49, v49, vcc
	v_cmp_ge_f32 vcc, v63, v164
	v_addc_co_u32 v5, vcc, v5, v5, vcc
	v_cmp_ge_f32 vcc, v62, v165
	v_addc_co_u32 v49, vcc, v49, v49, vcc
	v_cmp_ge_f32 vcc, v62, v164
	v_addc_co_u32 v5, vcc, v5, v5, vcc
	v_cmp_ge_f32 vcc, v61, v165
	v_addc_co_u32 v49, vcc, v49, v49, vcc
	v_cmp_ge_f32 vcc, v61, v164
	v_addc_co_u32 v5, vcc, v5, v5, vcc
	v_cmp_ge_f32 vcc, v60, v165
	v_addc_co_u32 v49, vcc, v49, v49, vcc
	v_cmp_ge_f32 vcc, v60, v164
	v_addc_co_u32 v5, vcc, v5, v5, vcc
	v_cmp_ge_f32 vcc, v59, v165
	v_addc_co_u32 v49, vcc, v49, v49, vcc
	v_cmp_ge_f32 vcc, v59, v164
	v_addc_co_u32 v5, vcc, v5, v5, vcc
	v_cmp_ge_f32 vcc, v58, v165
	v_addc_co_u32 v49, vcc, v49, v49, vcc
	v_cmp_ge_f32 vcc, v58, v164
	v_addc_co_u32 v5, vcc, v5, v5, vcc
	v_cmp_ge_f32 vcc, v57, v165
	v_addc_co_u32 v49, vcc, v49, v49, vcc
	v_cmp_ge_f32 vcc, v57, v164
	v_addc_co_u32 v5, vcc, v5, v5, vcc
	s_nop 0
	v_cmp_ge_f32 vcc, v56, v165
	v_addc_co_u32 v49, vcc, v49, v49, vcc
	s_nop 0
	v_cmp_ge_f32 vcc, v56, v164
	v_addc_co_u32 v5, vcc, v5, v5, vcc
	s_nop 0
	v_cmp_ge_f32 vcc, v55, v165
	v_addc_co_u32 v49, vcc, v49, v49, vcc
	s_nop 0
	v_cmp_ge_f32 vcc, v55, v164
	v_addc_co_u32 v5, vcc, v5, v5, vcc
	s_nop 0
	v_cmp_ge_f32 vcc, v54, v165
	v_addc_co_u32 v49, vcc, v49, v49, vcc
	s_nop 0
	v_cmp_ge_f32 vcc, v54, v164
	v_addc_co_u32 v5, vcc, v5, v5, vcc
	s_nop 0
	v_cmp_ge_f32 vcc, v53, v165
	v_addc_co_u32 v49, vcc, v49, v49, vcc
	s_nop 0
	v_cmp_ge_f32 vcc, v53, v164
	v_addc_co_u32 v5, vcc, v5, v5, vcc
	s_nop 0
	v_bitop3_b32 v3, v5, v49, v5 bitop3:0x30
	v_bitop3_b32 v5, v5, 15, v49 bitop3:0x40
	v_lshlrev_b32_e32 v7, 4, v3
	v_and_or_b32 v5, v7, s93, v5
	v_lshlrev_b32_e32 v7, 8, v3
	v_lshlrev_b32_e32 v9, 12, v3
	v_and_b32_e32 v7, 0xf0000, v7
	v_and_b32_e32 v9, 0xf000000, v9
	v_or3_b32 v48, v5, v7, v9
	v_cmp_ne_u32_e32 vcc, 0, v48
	s_and_b64 s[0:1], s[10:11], vcc
	s_and_saveexec_b64 s[18:19], s[0:1]
	s_cbranch_execz .LBB0_1195
	v_bcnt_u32_b32 v5, v48, 0
	ds_add_rtn_u32 v147, v221, v5
	v_and_b32_e32 v5, 1, v3
	v_cmp_eq_u32_e32 vcc, 1, v5
	s_and_saveexec_b64 s[14:15], vcc
	s_cbranch_execz .LBB0_1137
	s_waitcnt lgkmcnt(0)
	v_cmp_gt_u32_e32 vcc, s87, v147
	s_and_saveexec_b64 s[42:43], vcc
	s_cbranch_execz .LBB0_1136
	v_add_f32_e32 v0, 0, v53
	v_ashrrev_i32_e32 v252, 31, v0
	v_bitop3_b32 v0, v252, v0, s85 bitop3:0x36
	v_lshlrev_b64 v[148:149], 16, v[0:1]
	v_add_u32_e32 v0, s45, v142
	v_subrev_u32_e32 v0, 32, v0
	v_lshl_add_u32 v5, v147, 3, v136
	v_or_b32_e32 v148, v148, v0
	ds_write_b64 v5, v[148:149] offset:512

; #define LAS __attribute__((address_space(3)))
; __device__ __forceinline__ int crow(int r, int hi) { return (r & 3) + 8 * (r >> 2) + 4 * hi; }
; __device__ __forceinline__ unsigned fkey2(float v) { const unsigned u = __float_as_uint(v + 0.0f); return u ^ ((unsigned)((int)u >> 31) | 0x80000000u); }
; template <int PASS, bool DIAG> __device__ __forceinline__ void idx_half(unsigned& bits, unsigned& ebits, const f32x16& sc, int sbase, int tq, int r32, int hi, unsigned khi, unsigned klo, bool cand, LAS unsigned char* L) {
;     ...
;             for (int r = 0; r < 16; ++r) if ((ebits >> crow(r, 0)) & 1u) { const int s = sbase + crow(r, hi);
;                 if (slot < (unsigned)IDX_CAP) ((LAS unsigned long long*)(L + IL_CAND))[r32 * IDX_CAP + slot] = ((unsigned long long)fkey2(sc[r]) << 16) | (unsigned long long)(0xFFFFu - (unsigned)s);
.LBB0_1137:
	s_or_b64 exec, exec, s[14:15]
	v_and_b32_e32 v0, 2, v3
	v_cmp_ne_u32_e32 vcc, 0, v0
	s_and_saveexec_b64 s[14:15], vcc
	s_cbranch_execz .LBB0_1141
	s_waitcnt lgkmcnt(0)
	v_cmp_gt_u32_e32 vcc, s87, v147
	s_and_saveexec_b64 s[42:43], vcc
	s_cbranch_execz .LBB0_1140
	s_add_i32 s0, s16, 0xfffffe00
	v_mov_b32_e32 v47, v1
	s_xnor_b32 s0, s0, 32
	v_add_f32_e32 v46, 0, v54
	v_ashrrev_i32_e32 v252, 31, v46
	v_bitop3_b32 v46, v252, v46, s85 bitop3:0x36
	v_lshlrev_b64 v[46:47], 16, v[46:47]
	v_add_u32_e32 v0, s0, v138
	v_or_b32_e32 v46, v46, v0
	v_lshl_add_u32 v0, v147, 3, v136
	ds_write_b64 v0, v[46:47] offset:512

; #define LAS __attribute__((address_space(3)))
; __device__ __forceinline__ int crow(int r, int hi) { return (r & 3) + 8 * (r >> 2) + 4 * hi; }
; __device__ __forceinline__ unsigned fkey2(float v) { const unsigned u = __float_as_uint(v + 0.0f); return u ^ ((unsigned)((int)u >> 31) | 0x80000000u); }
; template <int PASS, bool DIAG> __device__ __forceinline__ void idx_half(unsigned& bits, unsigned& ebits, const f32x16& sc, int sbase, int tq, int r32, int hi, unsigned khi, unsigned klo, bool cand, LAS unsigned char* L) {
;     ...
;             for (int r = 0; r < 16; ++r) if ((ebits >> crow(r, 0)) & 1u) { const int s = sbase + crow(r, hi);
;                 if (slot < (unsigned)IDX_CAP) ((LAS unsigned long long*)(L + IL_CAND))[r32 * IDX_CAP + slot] = ((unsigned long long)fkey2(sc[r]) << 16) | (unsigned long long)(0xFFFFu - (unsigned)s);
.LBB0_1141:
	s_or_b64 exec, exec, s[14:15]
	v_and_b32_e32 v0, 4, v3
	v_cmp_ne_u32_e32 vcc, 0, v0
	s_and_saveexec_b64 s[14:15], vcc
	s_cbranch_execz .LBB0_1145
	s_waitcnt lgkmcnt(0)
	v_cmp_gt_u32_e32 vcc, s87, v147
	s_and_saveexec_b64 s[42:43], vcc
	s_cbranch_execz .LBB0_1144
	v_mov_b32_e32 v45, v1
	v_add_u32_e32 v0, s45, v140
	v_add_f32_e32 v44, 0, v55
	v_ashrrev_i32_e32 v252, 31, v44
	v_bitop3_b32 v44, v252, v44, s85 bitop3:0x36
	v_lshlrev_b64 v[44:45], 16, v[44:45]
	v_add_u32_e32 v0, 0xffdd, v0
	v_or_b32_e32 v44, v44, v0
	v_lshl_add_u32 v0, v147, 3, v136
	ds_write_b64 v0, v[44:45] offset:512

; #define LAS __attribute__((address_space(3)))
; __device__ __forceinline__ int crow(int r, int hi) { return (r & 3) + 8 * (r >> 2) + 4 * hi; }
; __device__ __forceinline__ unsigned fkey2(float v) { const unsigned u = __float_as_uint(v + 0.0f); return u ^ ((unsigned)((int)u >> 31) | 0x80000000u); }
; template <int PASS, bool DIAG> __device__ __forceinline__ void idx_half(unsigned& bits, unsigned& ebits, const f32x16& sc, int sbase, int tq, int r32, int hi, unsigned khi, unsigned klo, bool cand, LAS unsigned char* L) {
;     ...
;             for (int r = 0; r < 16; ++r) if ((ebits >> crow(r, 0)) & 1u) { const int s = sbase + crow(r, hi);
;                 if (slot < (unsigned)IDX_CAP) ((LAS unsigned long long*)(L + IL_CAND))[r32 * IDX_CAP + slot] = ((unsigned long long)fkey2(sc[r]) << 16) | (unsigned long long)(0xFFFFu - (unsigned)s);
.LBB0_1145:
	s_or_b64 exec, exec, s[14:15]
	v_and_b32_e32 v0, 8, v3
	v_cmp_ne_u32_e32 vcc, 0, v0
	s_and_saveexec_b64 s[14:15], vcc
	s_cbranch_execz .LBB0_1149
	s_waitcnt lgkmcnt(0)
	v_cmp_gt_u32_e32 vcc, s87, v147
	s_and_saveexec_b64 s[42:43], vcc
	s_cbranch_execz .LBB0_1148
	v_mov_b32_e32 v43, v1
	v_add_u32_e32 v0, s45, v140
	v_add_f32_e32 v42, 0, v56
	v_ashrrev_i32_e32 v252, 31, v42
	v_bitop3_b32 v42, v252, v42, s85 bitop3:0x36
	v_lshlrev_b64 v[42:43], 16, v[42:43]
	v_add_u32_e32 v0, 0xffdc, v0
	v_or_b32_e32 v42, v42, v0
	v_lshl_add_u32 v0, v147, 3, v136
	ds_write_b64 v0, v[42:43] offset:512

; #define LAS __attribute__((address_space(3)))
; __device__ __forceinline__ int crow(int r, int hi) { return (r & 3) + 8 * (r >> 2) + 4 * hi; }
; __device__ __forceinline__ unsigned fkey2(float v) { const unsigned u = __float_as_uint(v + 0.0f); return u ^ ((unsigned)((int)u >> 31) | 0x80000000u); }
; template <int PASS, bool DIAG> __device__ __forceinline__ void idx_half(unsigned& bits, unsigned& ebits, const f32x16& sc, int sbase, int tq, int r32, int hi, unsigned khi, unsigned klo, bool cand, LAS unsigned char* L) {
;     ...
;             for (int r = 0; r < 16; ++r) if ((ebits >> crow(r, 0)) & 1u) { const int s = sbase + crow(r, hi);
;                 if (slot < (unsigned)IDX_CAP) ((LAS unsigned long long*)(L + IL_CAND))[r32 * IDX_CAP + slot] = ((unsigned long long)fkey2(sc[r]) << 16) | (unsigned long long)(0xFFFFu - (unsigned)s);
.LBB0_1149:
	s_or_b64 exec, exec, s[14:15]
	v_and_b32_e32 v0, 16, v3
	v_cmp_ne_u32_e32 vcc, 0, v0
	s_and_saveexec_b64 s[14:15], vcc
	s_cbranch_execz .LBB0_1153
	s_waitcnt lgkmcnt(0)
	v_cmp_gt_u32_e32 vcc, s87, v147
	s_and_saveexec_b64 s[42:43], vcc
	s_cbranch_execz .LBB0_1152
	v_mov_b32_e32 v41, v1
	v_add_u32_e32 v0, s45, v140
	v_add_f32_e32 v40, 0, v57
	v_ashrrev_i32_e32 v252, 31, v40
	v_bitop3_b32 v40, v252, v40, s85 bitop3:0x36
	v_lshlrev_b64 v[40:41], 16, v[40:41]
	v_add_u32_e32 v0, 0xffd7, v0
	v_or_b32_e32 v40, v40, v0
	v_lshl_add_u32 v0, v147, 3, v136
	ds_write_b64 v0, v[40:41] offset:512

; #define LAS __attribute__((address_space(3)))
; __device__ __forceinline__ int crow(int r, int hi) { return (r & 3) + 8 * (r >> 2) + 4 * hi; }
; __device__ __forceinline__ unsigned fkey2(float v) { const unsigned u = __float_as_uint(v + 0.0f); return u ^ ((unsigned)((int)u >> 31) | 0x80000000u); }
; template <int PASS, bool DIAG> __device__ __forceinline__ void idx_half(unsigned& bits, unsigned& ebits, const f32x16& sc, int sbase, int tq, int r32, int hi, unsigned khi, unsigned klo, bool cand, LAS unsigned char* L) {
;     ...
;             for (int r = 0; r < 16; ++r) if ((ebits >> crow(r, 0)) & 1u) { const int s = sbase + crow(r, hi);
;                 if (slot < (unsigned)IDX_CAP) ((LAS unsigned long long*)(L + IL_CAND))[r32 * IDX_CAP + slot] = ((unsigned long long)fkey2(sc[r]) << 16) | (unsigned long long)(0xFFFFu - (unsigned)s);
.LBB0_1153:
	s_or_b64 exec, exec, s[14:15]
	v_and_b32_e32 v0, 32, v3
	v_cmp_ne_u32_e32 vcc, 0, v0
	s_and_saveexec_b64 s[14:15], vcc
	s_cbranch_execz .LBB0_1157
	s_waitcnt lgkmcnt(0)
	v_cmp_gt_u32_e32 vcc, s87, v147
	s_and_saveexec_b64 s[42:43], vcc
	s_cbranch_execz .LBB0_1156
	v_mov_b32_e32 v39, v1
	v_add_u32_e32 v0, s45, v140
	v_add_f32_e32 v38, 0, v58
	v_ashrrev_i32_e32 v252, 31, v38
	v_bitop3_b32 v38, v252, v38, s85 bitop3:0x36
	v_lshlrev_b64 v[38:39], 16, v[38:39]
	v_add_u32_e32 v0, 0xffd6, v0
	v_or_b32_e32 v38, v38, v0
	v_lshl_add_u32 v0, v147, 3, v136
	ds_write_b64 v0, v[38:39] offset:512

; #define LAS __attribute__((address_space(3)))
; __device__ __forceinline__ int crow(int r, int hi) { return (r & 3) + 8 * (r >> 2) + 4 * hi; }
; __device__ __forceinline__ unsigned fkey2(float v) { const unsigned u = __float_as_uint(v + 0.0f); return u ^ ((unsigned)((int)u >> 31) | 0x80000000u); }
; template <int PASS, bool DIAG> __device__ __forceinline__ void idx_half(unsigned& bits, unsigned& ebits, const f32x16& sc, int sbase, int tq, int r32, int hi, unsigned khi, unsigned klo, bool cand, LAS unsigned char* L) {
;     ...
;             for (int r = 0; r < 16; ++r) if ((ebits >> crow(r, 0)) & 1u) { const int s = sbase + crow(r, hi);
;                 if (slot < (unsigned)IDX_CAP) ((LAS unsigned long long*)(L + IL_CAND))[r32 * IDX_CAP + slot] = ((unsigned long long)fkey2(sc[r]) << 16) | (unsigned long long)(0xFFFFu - (unsigned)s);
.LBB0_1157:
	s_or_b64 exec, exec, s[14:15]
	v_and_b32_e32 v0, 64, v3
	v_cmp_ne_u32_e32 vcc, 0, v0
	s_and_saveexec_b64 s[14:15], vcc
	s_cbranch_execz .LBB0_1161
	s_waitcnt lgkmcnt(0)
	v_cmp_gt_u32_e32 vcc, s87, v147
	s_and_saveexec_b64 s[42:43], vcc
	s_cbranch_execz .LBB0_1160
	v_mov_b32_e32 v37, v1
	v_add_u32_e32 v0, s45, v140
	v_add_f32_e32 v36, 0, v59
	v_ashrrev_i32_e32 v252, 31, v36
	v_bitop3_b32 v36, v252, v36, s85 bitop3:0x36
	v_lshlrev_b64 v[36:37], 16, v[36:37]
	v_add_u32_e32 v0, 0xffd5, v0
	v_or_b32_e32 v36, v36, v0
	v_lshl_add_u32 v0, v147, 3, v136
	ds_write_b64 v0, v[36:37] offset:512

; #define LAS __attribute__((address_space(3)))
; __device__ __forceinline__ int crow(int r, int hi) { return (r & 3) + 8 * (r >> 2) + 4 * hi; }
; __device__ __forceinline__ unsigned fkey2(float v) { const unsigned u = __float_as_uint(v + 0.0f); return u ^ ((unsigned)((int)u >> 31) | 0x80000000u); }
; template <int PASS, bool DIAG> __device__ __forceinline__ void idx_half(unsigned& bits, unsigned& ebits, const f32x16& sc, int sbase, int tq, int r32, int hi, unsigned khi, unsigned klo, bool cand, LAS unsigned char* L) {
;     ...
;             for (int r = 0; r < 16; ++r) if ((ebits >> crow(r, 0)) & 1u) { const int s = sbase + crow(r, hi);
;                 if (slot < (unsigned)IDX_CAP) ((LAS unsigned long long*)(L + IL_CAND))[r32 * IDX_CAP + slot] = ((unsigned long long)fkey2(sc[r]) << 16) | (unsigned long long)(0xFFFFu - (unsigned)s);
.LBB0_1161:
	s_or_b64 exec, exec, s[14:15]
	v_and_b32_e32 v0, 0x80, v3
	v_cmp_ne_u32_e32 vcc, 0, v0
	s_and_saveexec_b64 s[14:15], vcc
	s_cbranch_execz .LBB0_1165
	s_waitcnt lgkmcnt(0)
	v_cmp_gt_u32_e32 vcc, s87, v147
	s_and_saveexec_b64 s[42:43], vcc
	s_cbranch_execz .LBB0_1164
	v_mov_b32_e32 v35, v1
	v_add_u32_e32 v0, s45, v140
	v_add_f32_e32 v34, 0, v60
	v_ashrrev_i32_e32 v252, 31, v34
	v_bitop3_b32 v34, v252, v34, s85 bitop3:0x36
	v_lshlrev_b64 v[34:35], 16, v[34:35]
	v_add_u32_e32 v0, 0xffd4, v0
	v_or_b32_e32 v34, v34, v0
	v_lshl_add_u32 v0, v147, 3, v136
	ds_write_b64 v0, v[34:35] offset:512

; #define LAS __attribute__((address_space(3)))
; __device__ __forceinline__ int crow(int r, int hi) { return (r & 3) + 8 * (r >> 2) + 4 * hi; }
; __device__ __forceinline__ unsigned fkey2(float v) { const unsigned u = __float_as_uint(v + 0.0f); return u ^ ((unsigned)((int)u >> 31) | 0x80000000u); }
; template <int PASS, bool DIAG> __device__ __forceinline__ void idx_half(unsigned& bits, unsigned& ebits, const f32x16& sc, int sbase, int tq, int r32, int hi, unsigned khi, unsigned klo, bool cand, LAS unsigned char* L) {
;     ...
;             for (int r = 0; r < 16; ++r) if ((ebits >> crow(r, 0)) & 1u) { const int s = sbase + crow(r, hi);
;                 if (slot < (unsigned)IDX_CAP) ((LAS unsigned long long*)(L + IL_CAND))[r32 * IDX_CAP + slot] = ((unsigned long long)fkey2(sc[r]) << 16) | (unsigned long long)(0xFFFFu - (unsigned)s);
.LBB0_1165:
	s_or_b64 exec, exec, s[14:15]
	v_and_b32_e32 v0, 0x100, v3
	v_cmp_ne_u32_e32 vcc, 0, v0
	s_and_saveexec_b64 s[14:15], vcc
	s_cbranch_execz .LBB0_1169
	s_waitcnt lgkmcnt(0)
	v_cmp_gt_u32_e32 vcc, s87, v147
	s_and_saveexec_b64 s[42:43], vcc
	s_cbranch_execz .LBB0_1168
	v_mov_b32_e32 v17, v1
	v_add_u32_e32 v0, s45, v140
	v_add_f32_e32 v16, 0, v61
	v_ashrrev_i32_e32 v252, 31, v16
	v_bitop3_b32 v16, v252, v16, s85 bitop3:0x36
	v_lshlrev_b64 v[16:17], 16, v[16:17]
	v_add_u32_e32 v0, 0xffcf, v0
	v_or_b32_e32 v16, v16, v0
	v_lshl_add_u32 v0, v147, 3, v136
	ds_write_b64 v0, v[16:17] offset:512

; #define LAS __attribute__((address_space(3)))
; __device__ __forceinline__ int crow(int r, int hi) { return (r & 3) + 8 * (r >> 2) + 4 * hi; }
; __device__ __forceinline__ unsigned fkey2(float v) { const unsigned u = __float_as_uint(v + 0.0f); return u ^ ((unsigned)((int)u >> 31) | 0x80000000u); }
; template <int PASS, bool DIAG> __device__ __forceinline__ void idx_half(unsigned& bits, unsigned& ebits, const f32x16& sc, int sbase, int tq, int r32, int hi, unsigned khi, unsigned klo, bool cand, LAS unsigned char* L) {
;     ...
;             for (int r = 0; r < 16; ++r) if ((ebits >> crow(r, 0)) & 1u) { const int s = sbase + crow(r, hi);
;                 if (slot < (unsigned)IDX_CAP) ((LAS unsigned long long*)(L + IL_CAND))[r32 * IDX_CAP + slot] = ((unsigned long long)fkey2(sc[r]) << 16) | (unsigned long long)(0xFFFFu - (unsigned)s);
.LBB0_1169:
	s_or_b64 exec, exec, s[14:15]
	v_and_b32_e32 v0, 0x200, v3
	v_cmp_ne_u32_e32 vcc, 0, v0
	s_and_saveexec_b64 s[14:15], vcc
	s_cbranch_execz .LBB0_1173
	s_waitcnt lgkmcnt(0)
	v_cmp_gt_u32_e32 vcc, s87, v147
	s_and_saveexec_b64 s[42:43], vcc
	s_cbranch_execz .LBB0_1172
	v_mov_b32_e32 v15, v1
	v_add_u32_e32 v0, s45, v140
	v_add_f32_e32 v14, 0, v62
	v_ashrrev_i32_e32 v252, 31, v14
	v_bitop3_b32 v14, v252, v14, s85 bitop3:0x36
	v_lshlrev_b64 v[14:15], 16, v[14:15]
	v_add_u32_e32 v0, 0xffce, v0
	v_or_b32_e32 v14, v14, v0
	v_lshl_add_u32 v0, v147, 3, v136
	ds_write_b64 v0, v[14:15] offset:512

; #define LAS __attribute__((address_space(3)))
; __device__ __forceinline__ int crow(int r, int hi) { return (r & 3) + 8 * (r >> 2) + 4 * hi; }
; __device__ __forceinline__ unsigned fkey2(float v) { const unsigned u = __float_as_uint(v + 0.0f); return u ^ ((unsigned)((int)u >> 31) | 0x80000000u); }
; template <int PASS, bool DIAG> __device__ __forceinline__ void idx_half(unsigned& bits, unsigned& ebits, const f32x16& sc, int sbase, int tq, int r32, int hi, unsigned khi, unsigned klo, bool cand, LAS unsigned char* L) {
;     ...
;             for (int r = 0; r < 16; ++r) if ((ebits >> crow(r, 0)) & 1u) { const int s = sbase + crow(r, hi);
;                 if (slot < (unsigned)IDX_CAP) ((LAS unsigned long long*)(L + IL_CAND))[r32 * IDX_CAP + slot] = ((unsigned long long)fkey2(sc[r]) << 16) | (unsigned long long)(0xFFFFu - (unsigned)s);
.LBB0_1173:
	s_or_b64 exec, exec, s[14:15]
	v_and_b32_e32 v0, 0x400, v3
	v_cmp_ne_u32_e32 vcc, 0, v0
	s_and_saveexec_b64 s[14:15], vcc
	s_cbranch_execz .LBB0_1177
	s_waitcnt lgkmcnt(0)
	v_cmp_gt_u32_e32 vcc, s87, v147
	s_and_saveexec_b64 s[42:43], vcc
	s_cbranch_execz .LBB0_1176
	v_mov_b32_e32 v13, v1
	v_add_u32_e32 v0, s45, v140
	v_add_f32_e32 v12, 0, v63
	v_ashrrev_i32_e32 v252, 31, v12
	v_bitop3_b32 v12, v252, v12, s85 bitop3:0x36
	v_lshlrev_b64 v[12:13], 16, v[12:13]
	v_add_u32_e32 v0, 0xffcd, v0
	v_or_b32_e32 v12, v12, v0
	v_lshl_add_u32 v0, v147, 3, v136
	ds_write_b64 v0, v[12:13] offset:512

; #define LAS __attribute__((address_space(3)))
; __device__ __forceinline__ int crow(int r, int hi) { return (r & 3) + 8 * (r >> 2) + 4 * hi; }
; __device__ __forceinline__ unsigned fkey2(float v) { const unsigned u = __float_as_uint(v + 0.0f); return u ^ ((unsigned)((int)u >> 31) | 0x80000000u); }
; template <int PASS, bool DIAG> __device__ __forceinline__ void idx_half(unsigned& bits, unsigned& ebits, const f32x16& sc, int sbase, int tq, int r32, int hi, unsigned khi, unsigned klo, bool cand, LAS unsigned char* L) {
;     ...
;             for (int r = 0; r < 16; ++r) if ((ebits >> crow(r, 0)) & 1u) { const int s = sbase + crow(r, hi);
;                 if (slot < (unsigned)IDX_CAP) ((LAS unsigned long long*)(L + IL_CAND))[r32 * IDX_CAP + slot] = ((unsigned long long)fkey2(sc[r]) << 16) | (unsigned long long)(0xFFFFu - (unsigned)s);
.LBB0_1177:
	s_or_b64 exec, exec, s[14:15]
	v_and_b32_e32 v0, 0x800, v3
	v_cmp_ne_u32_e32 vcc, 0, v0
	s_and_saveexec_b64 s[14:15], vcc
	s_cbranch_execz .LBB0_1181
	s_waitcnt lgkmcnt(0)
	v_cmp_gt_u32_e32 vcc, s87, v147
	s_and_saveexec_b64 s[42:43], vcc
	s_cbranch_execz .LBB0_1180
	v_mov_b32_e32 v11, v1
	v_add_u32_e32 v0, s45, v140
	v_add_f32_e32 v10, 0, v64
	v_ashrrev_i32_e32 v252, 31, v10
	v_bitop3_b32 v10, v252, v10, s85 bitop3:0x36
	v_lshlrev_b64 v[10:11], 16, v[10:11]
	v_add_u32_e32 v0, 0xffcc, v0
	v_or_b32_e32 v10, v10, v0
	v_lshl_add_u32 v0, v147, 3, v136
	ds_write_b64 v0, v[10:11] offset:512

; #define LAS __attribute__((address_space(3)))
; __device__ __forceinline__ int crow(int r, int hi) { return (r & 3) + 8 * (r >> 2) + 4 * hi; }
; __device__ __forceinline__ unsigned fkey2(float v) { const unsigned u = __float_as_uint(v + 0.0f); return u ^ ((unsigned)((int)u >> 31) | 0x80000000u); }
; template <int PASS, bool DIAG> __device__ __forceinline__ void idx_half(unsigned& bits, unsigned& ebits, const f32x16& sc, int sbase, int tq, int r32, int hi, unsigned khi, unsigned klo, bool cand, LAS unsigned char* L) {
;     ...
;             for (int r = 0; r < 16; ++r) if ((ebits >> crow(r, 0)) & 1u) { const int s = sbase + crow(r, hi);
;                 if (slot < (unsigned)IDX_CAP) ((LAS unsigned long long*)(L + IL_CAND))[r32 * IDX_CAP + slot] = ((unsigned long long)fkey2(sc[r]) << 16) | (unsigned long long)(0xFFFFu - (unsigned)s);
.LBB0_1181:
	s_or_b64 exec, exec, s[14:15]
	v_and_b32_e32 v0, 0x1000, v3
	v_cmp_ne_u32_e32 vcc, 0, v0
	s_and_saveexec_b64 s[14:15], vcc
	s_cbranch_execz .LBB0_1185
	s_waitcnt lgkmcnt(0)
	v_cmp_gt_u32_e32 vcc, s87, v147
	s_and_saveexec_b64 s[42:43], vcc
	s_cbranch_execz .LBB0_1184
	v_mov_b32_e32 v9, v1
	v_add_u32_e32 v0, s45, v140
	v_add_f32_e32 v8, 0, v65
	v_ashrrev_i32_e32 v252, 31, v8
	v_bitop3_b32 v8, v252, v8, s85 bitop3:0x36
	v_lshlrev_b64 v[8:9], 16, v[8:9]
	v_add_u32_e32 v0, 0xffc7, v0
	v_or_b32_e32 v8, v8, v0
	v_lshl_add_u32 v0, v147, 3, v136
	ds_write_b64 v0, v[8:9] offset:512

; #define LAS __attribute__((address_space(3)))
; __device__ __forceinline__ int crow(int r, int hi) { return (r & 3) + 8 * (r >> 2) + 4 * hi; }
; __device__ __forceinline__ unsigned fkey2(float v) { const unsigned u = __float_as_uint(v + 0.0f); return u ^ ((unsigned)((int)u >> 31) | 0x80000000u); }
; template <int PASS, bool DIAG> __device__ __forceinline__ void idx_half(unsigned& bits, unsigned& ebits, const f32x16& sc, int sbase, int tq, int r32, int hi, unsigned khi, unsigned klo, bool cand, LAS unsigned char* L) {
;     ...
;             for (int r = 0; r < 16; ++r) if ((ebits >> crow(r, 0)) & 1u) { const int s = sbase + crow(r, hi);
;                 if (slot < (unsigned)IDX_CAP) ((LAS unsigned long long*)(L + IL_CAND))[r32 * IDX_CAP + slot] = ((unsigned long long)fkey2(sc[r]) << 16) | (unsigned long long)(0xFFFFu - (unsigned)s);
.LBB0_1185:
	s_or_b64 exec, exec, s[14:15]
	v_and_b32_e32 v0, 0x2000, v3
	v_cmp_ne_u32_e32 vcc, 0, v0
	s_and_saveexec_b64 s[14:15], vcc
	s_cbranch_execz .LBB0_1189
	s_waitcnt lgkmcnt(0)
	v_cmp_gt_u32_e32 vcc, s87, v147
	s_and_saveexec_b64 s[42:43], vcc
	s_cbranch_execz .LBB0_1188
	v_mov_b32_e32 v7, v1
	v_add_u32_e32 v0, s45, v140
	v_add_f32_e32 v6, 0, v144
	v_ashrrev_i32_e32 v252, 31, v6
	v_bitop3_b32 v6, v252, v6, s85 bitop3:0x36
	v_lshlrev_b64 v[6:7], 16, v[6:7]
	v_add_u32_e32 v0, 0xffc6, v0
	v_or_b32_e32 v6, v6, v0
	v_lshl_add_u32 v0, v147, 3, v136
	ds_write_b64 v0, v[6:7] offset:512

; #define LAS __attribute__((address_space(3)))
; __device__ __forceinline__ int crow(int r, int hi) { return (r & 3) + 8 * (r >> 2) + 4 * hi; }
; __device__ __forceinline__ unsigned fkey2(float v) { const unsigned u = __float_as_uint(v + 0.0f); return u ^ ((unsigned)((int)u >> 31) | 0x80000000u); }
; template <int PASS, bool DIAG> __device__ __forceinline__ void idx_half(unsigned& bits, unsigned& ebits, const f32x16& sc, int sbase, int tq, int r32, int hi, unsigned khi, unsigned klo, bool cand, LAS unsigned char* L) {
;     ...
;             for (int r = 0; r < 16; ++r) if ((ebits >> crow(r, 0)) & 1u) { const int s = sbase + crow(r, hi);
;                 if (slot < (unsigned)IDX_CAP) ((LAS unsigned long long*)(L + IL_CAND))[r32 * IDX_CAP + slot] = ((unsigned long long)fkey2(sc[r]) << 16) | (unsigned long long)(0xFFFFu - (unsigned)s);
.LBB0_1189:
	s_or_b64 exec, exec, s[14:15]
	v_and_b32_e32 v0, 0x4000, v3
	v_cmp_ne_u32_e32 vcc, 0, v0
	s_and_saveexec_b64 s[14:15], vcc
	s_cbranch_execz .LBB0_1193
	s_waitcnt lgkmcnt(0)
	v_cmp_gt_u32_e32 vcc, s87, v147
	s_and_saveexec_b64 s[42:43], vcc
	s_cbranch_execz .LBB0_1192
	v_mov_b32_e32 v5, v1
	v_add_u32_e32 v0, s45, v140
	v_add_f32_e32 v4, 0, v145
	v_ashrrev_i32_e32 v252, 31, v4
	v_bitop3_b32 v4, v252, v4, s85 bitop3:0x36
	v_lshlrev_b64 v[4:5], 16, v[4:5]
	v_add_u32_e32 v0, 0xffc5, v0
	v_or_b32_e32 v4, v4, v0
	v_lshl_add_u32 v0, v147, 3, v136
	ds_write_b64 v0, v[4:5] offset:512

; #define LAS __attribute__((address_space(3)))
; __device__ __forceinline__ int crow(int r, int hi) { return (r & 3) + 8 * (r >> 2) + 4 * hi; }
; __device__ __forceinline__ unsigned fkey2(float v) { const unsigned u = __float_as_uint(v + 0.0f); return u ^ ((unsigned)((int)u >> 31) | 0x80000000u); }
; template <int PASS, bool DIAG> __device__ __forceinline__ void idx_half(unsigned& bits, unsigned& ebits, const f32x16& sc, int sbase, int tq, int r32, int hi, unsigned khi, unsigned klo, bool cand, LAS unsigned char* L) {
;     ...
;             for (int r = 0; r < 16; ++r) if ((ebits >> crow(r, 0)) & 1u) { const int s = sbase + crow(r, hi);
;                 if (slot < (unsigned)IDX_CAP) ((LAS unsigned long long*)(L + IL_CAND))[r32 * IDX_CAP + slot] = ((unsigned long long)fkey2(sc[r]) << 16) | (unsigned long long)(0xFFFFu - (unsigned)s);
.LBB0_1193:
	s_or_b64 exec, exec, s[14:15]
	v_and_b32_e32 v0, 0x8000, v3
	v_cmp_ne_u32_e32 vcc, 0, v0
	s_waitcnt lgkmcnt(0)
	v_cmp_gt_u32_e64 s[14:15], s87, v147
	s_and_b64 s[0:1], vcc, s[14:15]
	s_and_b64 exec, exec, s[0:1]
	s_cbranch_execz .LBB0_1195
	v_mov_b32_e32 v3, v1
	v_add_u32_e32 v0, s45, v140
	v_add_f32_e32 v2, 0, v146
	v_ashrrev_i32_e32 v252, 31, v2
	v_bitop3_b32 v2, v252, v2, s85 bitop3:0x36
	v_lshlrev_b64 v[2:3], 16, v[2:3]
	v_add_u32_e32 v0, 0xffc4, v0
	v_or_b32_e32 v2, v2, v0
	v_lshl_add_u32 v0, v147, 3, v136
	ds_write_b64 v0, v[2:3] offset:512

; #define LAS __attribute__((address_space(3)))
; __device__ __forceinline__ void dsa_qk(f32x16& p0, f32x16& p1, const LAS char* kp, const bf16x8 (&qr)[4], unsigned long long mw, int hi, float mref, const LAS char* tbl) {
;     ...
;     const unsigned mlo = (unsigned)mw >> (4 * hi), mhi = (unsigned)(mw >> 32) >> (4 * hi), negm = __float_as_uint(-mref);
;     if (tbl) {
; #pragma unroll
;         for (int i = 0; i < 4; ++i) { const u32x4 a = *(const LAS u32x4*)(tbl + ((mlo >> (8 * i)) & 15u) * 16u), b = *(const LAS u32x4*)(tbl + ((mhi >> (8 * i)) & 15u) * 16u);
; #pragma unroll
;             for (int e = 0; e < 4; ++e) { p0[4 * i + e] = __uint_as_float(a[e]); p1[4 * i + e] = __uint_as_float(b[e]); } }
; __device__ __forceinline__ void dsa_block_unit(int b, int g, int m  , const bf16_t* Q, const bf16_t* K, const bf16_t* V, const unsigned long long* mask, bf16_t* O, LAS char* L, int wid, int lane, float sbound  ) {
;     ...
;     bf16x8 qr[4];
; #pragma unroll
;     for (int d0 = 0; d0 < 4; ++d0) qr[d0] = *(const bf16x8*)(Qw + (size_t)r32 * 512 + 16 * d0 + 8 * hi);
;     f32x16 o[2]; o[0] = f32x16{}; o[1] = f32x16{};
;     const bool fixed = sbound > 0.f;
;     float mref = fixed ? sbound : 0.f, lsum = 0.f;
;     LAS float* wsf = (LAS float*)(L + DL_F + wid * 256);
;     const unsigned kvoff = (unsigned)lane * 256u;
;     const unsigned vvoff = (unsigned)((lane >> 2) * 128 + (lane & 3) * 8) * 2u;
;     const bf16_t* Kw = Kg + wid * 8; const bf16_t* Vw = Vg + (size_t)(16 * (wid & 3)) * 128 + (wid >> 2) * 32;
;     const unsigned kdst = (unsigned)(size_t)(L + DL_K) + wid * 1024u, vdst = (unsigned)(size_t)(L + DL_V) + wid * 1024u;
;     const LAS char* kp0 = L + DL_K + hi * 1024 + r32 * 16;
;     const LAS char* vp0 = L + DL_V + ((lane >> 4) & 1) * 32 + (lane & 3) * 8 + (4 * hi + ((lane & 15) >> 2)) * 64;
;     glds16_s(Kw, kvoff, kdst); glds16_s(Vw, vvoff, vdst);
;     if (jd >= 1) { glds16_s(Kw + (size_t)64 * 128, kvoff, kdst + 8192); glds16_s(Vw + (size_t)64 * 128, vvoff, vdst + 8192); }
;     unsigned long long mwn = mrow[0];
;     unsigned long long mwn2 = (jd >= 1) ? mrow[1] : 0ull;
;     asm volatile("s_waitcnt vmcnt(0) lgkmcnt(0)\n\ts_barrier" ::: "memory");
;     const LAS char* tblp = L + DL_T;
;     f32x16 pa0, pa1, pb0, pb1; dsa_qk(pa0, pa1, kp0, qr, mwn, hi, mref, fixed ? tblp : (const LAS char*)nullptr);
.LBB0_1674:
	s_or_b64 exec, exec, s[22:23]
.LBB0_1675:
	s_waitcnt vmcnt(0)
	s_waitcnt vmcnt(0)
.LBB0_1676:
	s_or_b64 exec, exec, s[16:17]
.LBB0_1677:
	s_lshl_b32 s0, s54, 6
	s_ashr_i32 s21, s20, 31
	s_bfe_u32 s16, s42, 0x10005
	v_readlane_b32 s2, v254, 55
	s_add_i32 s0, s0, s61
	s_lshl_b64 s[22:23], s[20:21], 12
	v_readlane_b32 s3, v254, 56
	s_add_u32 s28, s22, s0
	s_mov_b32 s1, s3
	s_addc_u32 s29, s23, 0
	s_mov_b64 s[70:71], s[0:1]
	s_lshl_b64 s[0:1], s[28:29], 10
	s_add_u32 s0, s43, s0
	s_addc_u32 s1, s44, s1
	s_lshl_b32 s2, s16, 8
	v_readlane_b32 s3, v254, 24
	s_or_b32 s2, s2, s3
	s_lshl_b32 s52, s2, 1
	s_add_u32 s0, s0, s52
	s_addc_u32 s1, s1, 0
	s_lshl_b64 s[2:3], s[20:21], 20
	s_add_u32 s17, s47, s2
	s_addc_u32 s18, s48, s3
	v_lshl_add_u64 v[4:5], s[0:1], 0, v[152:153]
	s_add_u32 s0, s45, s2
	s_addc_u32 s1, s46, s3
	s_lshl_b32 s2, s16, 7
	s_add_u32 s0, s0, s2
	s_addc_u32 s1, s1, 0
	s_add_u32 s2, s17, s2
	s_addc_u32 s3, s18, 0
	v_readlane_b32 s16, v254, 51
	s_add_u32 s16, s0, s16
	s_addc_u32 s17, s1, 0
	v_readlane_b32 s0, v254, 52
	s_add_u32 s0, s2, s0
	s_addc_u32 s1, s3, 0
	s_lshl_b32 s2, s61, 1
	s_add_u32 s18, s0, s2
	v_lshlrev_b32_e32 v0, 1, v154
	s_addc_u32 s19, s1, 0
	v_lshl_add_u64 v[4:5], v[4:5], 0, v[0:1]
	s_add_u32 s24, s18, 0x4000
	s_barrier
	global_load_dwordx4 v[98:101], v[4:5], off
	global_load_dwordx4 v[102:105], v[4:5], off offset:32
	global_load_dwordx4 v[106:109], v[4:5], off offset:64
	global_load_dwordx4 v[110:113], v[4:5], off offset:96
	s_nop 4
	s_mov_b32 s0, m0
	s_mov_b32 m0, s63
	s_nop 0
	global_load_lds_dwordx4 v172, s[16:17]
	s_mov_b32 m0, s0
	s_addc_u32 s25, s19, 0
	v_mov_b32_e32 v3, s29
	v_or_b32_e32 v2, s28, v150
	s_nop 4
	s_mov_b32 s0, m0
	s_mov_b32 m0, s64
	s_nop 0
	global_load_lds_dwordx4 v173, s[18:19]
	s_mov_b32 m0, s0
	s_add_u32 s26, s16, 0x4000
	v_lshlrev_b64 v[2:3], 9, v[2:3]
	s_addc_u32 s27, s17, 0
	v_readlane_b32 s1, v254, 29
	s_nop 4
	s_mov_b32 s0, m0
	s_mov_b32 m0, s1
	s_nop 0
	global_load_lds_dwordx4 v172, s[26:27]
	s_mov_b32 m0, s0
	v_lshl_add_u64 v[2:3], s[12:13], 0, v[2:3]
	v_readlane_b32 s1, v254, 28
	s_nop 4
	s_mov_b32 s0, m0
	s_mov_b32 m0, s1
	s_nop 0
	global_load_lds_dwordx4 v173, s[24:25]
	s_mov_b32 m0, s0
	global_load_dwordx4 v[114:117], v[2:3], off sc1
	s_waitcnt vmcnt(0) lgkmcnt(0)
	s_barrier
	ds_read_b128 v[30:33], v174
	ds_read_b128 v[26:29], v174 offset:512
	ds_read_b128 v[22:25], v174 offset:2048
	ds_read_b128 v[2:5], v174 offset:2560
	ds_read_b128 v[6:9], v174 offset:4096
	ds_read_b128 v[10:13], v174 offset:4608
	ds_read_b128 v[14:17], v174 offset:6144
	ds_read_b128 v[18:21], v174 offset:6656
	s_waitcnt vmcnt(0)
	v_lshrrev_b32_e32 v67, v176, v114
	v_lshrrev_b32_e32 v66, v176, v115
	s_and_saveexec_b64 s[0:1], s[4:5]
	s_xor_b64 s[30:31], exec, s[0:1]
	s_cbranch_execz .LBB0_1679
	v_lshlrev_b32_e32 v34, 4, v67
	v_lshlrev_b32_e32 v35, 4, v66
	v_and_b32_e32 v34, 0xf0, v34
	s_add_i32 s0, 0, 0x14800
	v_and_b32_e32 v35, 0xf0, v35
	v_add_u32_e32 v34, s0, v34
	v_add_u32_e32 v38, s0, v35
	ds_read_b128 v[34:37], v34
	ds_read_b128 v[50:53], v38
	v_lshrrev_b32_e32 v38, 4, v67
	v_lshrrev_b32_e32 v39, 4, v66
	v_and_b32_e32 v38, 0xf0, v38
	v_and_b32_e32 v39, 0xf0, v39
	v_add_u32_e32 v38, s0, v38
	v_add_u32_e32 v42, s0, v39
	ds_read_b128 v[38:41], v38
	ds_read_b128 v[54:57], v42
	v_lshrrev_b32_e32 v42, 12, v67
	v_lshrrev_b32_e32 v43, 12, v66
	v_and_b32_e32 v42, 0xf0, v42
	v_and_b32_e32 v43, 0xf0, v43
	v_add_u32_e32 v42, s0, v42
	v_add_u32_e32 v46, s0, v43
	ds_read_b128 v[42:45], v42
	ds_read_b128 v[58:61], v46
	v_lshrrev_b32_e32 v46, 20, v67
	v_lshrrev_b32_e32 v47, 20, v66
	v_and_b32_e32 v46, 0xf0, v46
	v_and_b32_e32 v47, 0xf0, v47
	v_add_u32_e32 v46, s0, v46
	v_add_u32_e32 v62, s0, v47
	ds_read_b128 v[46:49], v46
	ds_read_b128 v[62:65], v62

; __device__ __forceinline__ void dsa_block_unit(int b, int g, int m  , const bf16_t* Q, const bf16_t* K, const bf16_t* V, const unsigned long long* mask, bf16_t* O, LAS char* L, int wid, int lane, float sbound  ) {
;     ...
;     for (int j = 0; j <= jd; j += 2) {
;         if (j + 2 <= jd) { glds16_s(Kw + (size_t)(j + 2) * 64 * 128, kvoff, kdst + sn2); glds16_s(Vw + (size_t)(j + 2) * 64 * 128, vvoff, vdst + sn2); mwn2 = mrow[j + 2]; }
;         dsa_step(pa0, pa1, pb0, pb1, j < jd, kp0 + sn, vp0 + sc, qr, mwn, o, mref, lsum, wsf, r32, hi, fixed, tblp);
.LBB0_1684:
	s_add_i32 s60, s58, -1
	s_mov_b32 s59, s0
	s_cmp_gt_u32 s60, s54
	s_waitcnt vmcnt(0)
	v_mov_b64_e32 v[170:171], v[116:117]
	s_cbranch_scc1 .LBB0_1686
	s_add_u32 s0, s16, s30
	s_addc_u32 s1, s17, s31
	s_add_u32 s0, s0, 0x8000
	s_addc_u32 s1, s1, 0
	s_add_i32 s33, s59, s63
	s_add_u32 s2, s18, s30
	s_addc_u32 s3, s19, s31
	s_add_u32 s2, s2, 0x8000
	s_nop 4
	s_mov_b32 s35, m0
	s_mov_b32 m0, s33
	s_nop 0
	global_load_lds_dwordx4 v172, s[0:1]
	s_mov_b32 m0, s35
	s_addc_u32 s3, s3, 0
	s_add_i32 s34, s59, s64
	s_nop 4
	s_mov_b32 s0, m0
	s_mov_b32 m0, s34
	s_nop 0
	global_load_lds_dwordx4 v173, s[2:3]
	s_mov_b32 m0, s0
	global_load_dwordx2 v[170:171], v[168:169], off offset:-8 sc1

; #define LDS_WAIT() asm volatile("s_waitcnt lgkmcnt(0)" ::: "memory")
; __device__ __forceinline__ int crow(int r, int hi) { return (r & 3) + 8 * (r >> 2) + 4 * hi; }
; __device__ __forceinline__ void dsa_step(f32x16& c0, f32x16& c1, f32x16& n0, f32x16& n1, const bool have_n, const LAS char* kpn, const LAS char* vpc, const bf16x8 (&qr)[4], unsigned long long mwn, ...
;     ...
;     f32x2 ps2 = {0.f, 0.f};
; #pragma unroll
;     for (int r = 0; r < 16; r += 2) { c0[r] = __builtin_amdgcn_exp2f(c0[r]); c0[r + 1] = __builtin_amdgcn_exp2f(c0[r + 1]); c1[r] = __builtin_amdgcn_exp2f(c1[r]); c1[r + 1] = __builtin_amdgcn_exp2f(c1[r + 1]);
;         ps2 += (f32x2){c0[r], c0[r + 1]}; ps2 += (f32x2){c1[r], c1[r + 1]}; }
;     lsum += ps2[0] + ps2[1];
;     if (resc) { LDS_WAIT();
; #pragma unroll
;         for (int r = 0; r < 16; ++r) { const float f = wsf[crow(r, hi)]; o[0][r] *= f; o[1][r] *= f; } }
;     pv_mma(o, vf, c0, c1);
;     asm volatile("s_waitcnt vmcnt(0) lgkmcnt(0)\n\ts_barrier" ::: "memory");
; __device__ __forceinline__ void dsa_block_unit(int b, int g, int m  , const bf16_t* Q, const bf16_t* K, const bf16_t* V, const unsigned long long* mask, bf16_t* O, LAS char* L, int wid, int lane, float sbound  ) {
;     ...
;         if (j == jd) break;
;         { const int t_ = sc; sc = sn; sn = sn2; sn2 = t_; } mwn = mwn2;
;         if (j + 3 <= jd) { glds16_s(Kw + (size_t)(j + 3) * 64 * 128, kvoff, kdst + sn2); glds16_s(Vw + (size_t)(j + 3) * 64 * 128, vvoff, vdst + sn2); mwn2 = mrow[j + 3]; }
;         dsa_step(pb0, pb1, pa0, pa1, j + 1 < jd, kp0 + sn, vp0 + sc, qr, mwn, o, mref, lsum, wsf, r32, hi, fixed, tblp);
.LBB0_1696:
	s_or_b64 exec, exec, s[34:35]
	v_exp_f32_e32 v34, v34
	v_exp_f32_e32 v35, v35
	v_exp_f32_e32 v36, v36
	v_exp_f32_e32 v37, v37
	v_exp_f32_e32 v38, v38
	v_exp_f32_e32 v39, v39
	v_exp_f32_e32 v40, v40
	v_exp_f32_e32 v41, v41
	v_cvt_pk_bf16_f32 v146, v34, v35
	v_cvt_pk_bf16_f32 v147, v36, v37
	v_cvt_pk_bf16_f32 v148, v38, v39
	v_cvt_pk_bf16_f32 v149, v40, v41
	v_exp_f32_e32 v42, v42
	v_exp_f32_e32 v43, v43
	v_exp_f32_e32 v44, v44
	v_exp_f32_e32 v45, v45
	v_exp_f32_e32 v46, v46
	v_exp_f32_e32 v47, v47
	v_exp_f32_e32 v48, v48
	v_exp_f32_e32 v49, v49
	s_waitcnt lgkmcnt(14)
	v_mfma_f32_32x32x16_bf16 v[2:17], v[146:149], v[142:145], v[2:17]
	v_exp_f32_e32 v50, v50
	v_exp_f32_e32 v51, v51
	v_cvt_pk_bf16_f32 v142, v42, v43
	v_cvt_pk_bf16_f32 v143, v44, v45
	v_cvt_pk_bf16_f32 v144, v46, v47
	v_cvt_pk_bf16_f32 v145, v48, v49
	v_exp_f32_e32 v52, v52
	s_waitcnt lgkmcnt(10)
	v_mfma_f32_32x32x16_bf16 v[18:33], v[146:149], v[138:141], v[18:33]
	v_exp_f32_e32 v53, v53
	v_pk_add_f32 v[186:187], v[34:35], 0 op_sel_hi:[1,0]
	v_exp_f32_e32 v54, v54
	v_pk_add_f32 v[186:187], v[50:51], v[186:187]
	v_exp_f32_e32 v55, v55
	v_exp_f32_e32 v56, v56
	v_exp_f32_e32 v57, v57
	v_mfma_f32_32x32x16_bf16 v[2:17], v[142:145], v[134:137], v[2:17]
	v_add_f32_e64 v134, v186, v36
	v_add_f32_e64 v135, v187, v37
	v_cvt_pk_bf16_f32 v136, v54, v55
	v_add_f32_e64 v134, v52, v134
	v_add_f32_e64 v135, v53, v135
	v_cvt_pk_bf16_f32 v137, v56, v57
	v_pk_add_f32 v[134:135], v[134:135], v[38:39]
	v_exp_f32_e32 v58, v58
	v_pk_add_f32 v[138:139], v[54:55], v[134:135]
	s_waitcnt lgkmcnt(8)
	v_mfma_f32_32x32x16_bf16 v[18:33], v[142:145], v[130:133], v[18:33]
	v_cvt_pk_bf16_f32 v134, v50, v51
	v_cvt_pk_bf16_f32 v135, v52, v53
	v_exp_f32_e32 v59, v59
	v_exp_f32_e32 v60, v60
	v_exp_f32_e32 v61, v61
	v_exp_f32_e32 v62, v62
	v_exp_f32_e32 v63, v63
	v_exp_f32_e32 v64, v64
	v_exp_f32_e32 v65, v65
	s_waitcnt lgkmcnt(6)
	v_mfma_f32_32x32x16_bf16 v[2:17], v[134:137], v[126:129], v[2:17]
	v_cvt_pk_bf16_f32 v126, v58, v59
	v_cvt_pk_bf16_f32 v127, v60, v61
	v_cvt_pk_bf16_f32 v128, v62, v63
	v_cvt_pk_bf16_f32 v129, v64, v65
	v_add_f32_e64 v130, v138, v40
	v_add_f32_e64 v131, v139, v41
	s_waitcnt vmcnt(0) lgkmcnt(0)
	s_barrier
	s_add_i32 s0, s21, s58
	s_waitcnt lgkmcnt(2)
	v_mfma_f32_32x32x16_bf16 v[18:33], v[134:137], v[122:125], v[18:33]
	v_add_f32_e64 v130, v56, v130
	v_add_f32_e64 v131, v57, v131
	s_cmp_eq_u32 s0, 3
	v_add_f32_e64 v122, v130, v42
	v_add_f32_e64 v123, v131, v43
	v_readfirstlane_b32 s36, v0
	v_pk_add_f32 v[122:123], v[58:59], v[122:123]
	v_readfirstlane_b32 s37, v1
	v_pk_add_f32 v[122:123], v[122:123], v[44:45]
	v_mfma_f32_32x32x16_bf16 v[2:17], v[126:129], v[118:121], v[2:17]
	v_add_f32_e64 v122, v60, v122
	v_add_f32_e64 v123, v61, v123
	v_add_f32_e64 v118, v122, v46
	v_add_f32_e64 v119, v123, v47
	v_add_f32_e64 v118, v62, v118
	v_add_f32_e64 v119, v63, v119
	v_pk_add_f32 v[118:119], v[118:119], v[48:49]
	s_waitcnt lgkmcnt(0)
	v_mfma_f32_32x32x16_bf16 v[18:33], v[126:129], v[114:117], v[18:33]
	v_add_f32_e64 v118, v64, v118
	v_add_f32_e64 v119, v65, v119
	v_add_f32_e32 v118, v118, v119
	v_add_f32_e32 v157, v157, v118
	s_cbranch_scc1 .LBB0_1682
	s_cmp_gt_u32 s58, s54
	s_waitcnt vmcnt(0)
	v_mov_b64_e32 v[116:117], v[170:171]
	s_cbranch_scc1 .LBB0_1699
	s_add_u32 s0, s16, s30
	s_addc_u32 s1, s17, s31
	s_add_u32 s0, s0, 0xc000
	s_addc_u32 s1, s1, 0
	s_add_i32 s33, s55, s63
	s_add_u32 s2, s18, s30
	s_addc_u32 s3, s19, s31
	s_add_u32 s2, s2, 0xc000
	s_nop 4
	s_mov_b32 s35, m0
	s_mov_b32 m0, s33
	s_nop 0
	global_load_lds_dwordx4 v172, s[0:1]
	s_mov_b32 m0, s35
	s_addc_u32 s3, s3, 0
	s_add_i32 s34, s55, s64
	s_nop 4
	s_mov_b32 s0, m0
	s_mov_b32 m0, s34
	s_nop 0
	global_load_lds_dwordx4 v173, s[2:3]
	s_mov_b32 m0, s0
	global_load_dwordx2 v[116:117], v[168:169], off sc1

; __device__ __forceinline__ int lane_id() { int l; asm volatile("v_mbcnt_lo_u32_b32 %0, -1, 0\n\tv_mbcnt_hi_u32_b32 %0, -1, %0" : "=v"(l)); return l; }
; __device__ __forceinline__ unsigned xb_ld(unsigned* p)              { return __hip_atomic_load(p, __ATOMIC_RELAXED, __HIP_MEMORY_SCOPE_AGENT); }
; #define XB_SPIN(cond, bar) do { unsigned _sp = 0; while (cond) { __builtin_amdgcn_s_sleep(1); \
;     if ((++_sp & 255u) == 0u) { if (xb_ld(&(bar)[XB_TMO])) break; if (_sp > XB_SPIN_CAP) { atomicAdd(&(bar)[XB_TMO], 1u); break; } } } } while (0)
; __device__ __forceinline__ unsigned char* karg_ws() { return (unsigned char*)(GAS unsigned char*)karg_u64<15>(); }
; __device__ __forceinline__ void mflag_wait(int b, int m64, unsigned tag, int wave_s) {
;     if (wave_s == 0 && lane_id() == 0) {
;         unsigned* bar = (unsigned*)(karg_ws() + WS_CTL) + 4096; unsigned* f = (unsigned*)(karg_ws() + WS_CTL) + CTL_MFLAG + 16 * (128 * b + 2 * m64);
;         XB_SPIN(xb_ld(f) < tag || xb_ld(f + 16) < tag, bar);
;         __builtin_amdgcn_fence(__ATOMIC_ACQUIRE, "agent");
;         asm volatile("s_waitcnt vmcnt(0)" ::: "memory");
;     }
;     __syncthreads();
.LBB0_1740:
	s_or_b64 exec, exec, s[28:29]
.LBB0_1741:
	s_waitcnt vmcnt(0)
	s_waitcnt vmcnt(0)
.LBB0_1742:
	s_or_b64 exec, exec, s[10:11]

; __device__ __forceinline__ void dsa_block_unit(int b, int g, int m  , const bf16_t* Q, const bf16_t* K, const bf16_t* V, const unsigned long long* mask, bf16_t* O, LAS char* L, int wid, int lane, float sbound  ) {
;     ...
;     glds16_s(Kw, kvoff, kdst); glds16_s(Vw, vvoff, vdst);
;     if (jd >= 1) { glds16_s(Kw + (size_t)64 * 128, kvoff, kdst + 8192); glds16_s(Vw + (size_t)64 * 128, vvoff, vdst + 8192); }
;     unsigned long long mwn = mrow[0];
;     unsigned long long mwn2 = (jd >= 1) ? mrow[1] : 0ull;
.LBB0_1745:
	v_mov_b32_e32 v3, s11
	v_or_b32_e32 v2, s10, v150
	v_lshlrev_b64 v[2:3], 9, v[2:3]
	v_lshl_add_u64 v[2:3], s[12:13], 0, v[2:3]
	global_load_dwordx2 v[34:35], v[2:3], off sc1
	s_andn2_b64 vcc, exec, s[20:21]
	s_cbranch_vccnz .LBB0_1747
	global_load_dwordx2 v[148:149], v[2:3], off offset:8 sc1
	s_branch .LBB0_1748

; __device__ __forceinline__ void dsa_block_unit(int b, int g, int m  , const bf16_t* Q, const bf16_t* K, const bf16_t* V, const unsigned long long* mask, bf16_t* O, LAS char* L, int wid, int lane, float sbound  ) {
;     ...
;     for (int j = 0; j <= jd; j += 2) {
;         if (j + 2 <= jd) { glds16_s(Kw + (size_t)(j + 2) * 64 * 128, kvoff, kdst + sn2); glds16_s(Vw + (size_t)(j + 2) * 64 * 128, vvoff, vdst + sn2); mwn2 = mrow[j + 2]; }
;         dsa_step(pa0, pa1, pb0, pb1, j < jd, kp0 + sn, vp0 + sc, qr, mwn, o, mref, lsum, wsf, r32, hi, fixed, tblp);
.LBB0_1755:
	s_add_i32 s37, s35, -1
	s_mov_b32 s36, s0
	s_cmp_gt_u32 s37, s53
	s_waitcnt vmcnt(0)
	v_mov_b64_e32 v[166:167], v[148:149]
	s_cbranch_scc1 .LBB0_1757
	s_add_u32 s0, s16, s20
	s_addc_u32 s1, s17, s21
	s_add_u32 s0, s0, 0x8000
	s_addc_u32 s1, s1, 0
	s_add_i32 s22, s36, s63
	s_add_u32 s2, s18, s20
	s_addc_u32 s3, s19, s21
	s_add_u32 s2, s2, 0x8000
	s_nop 4
	s_mov_b32 s24, m0
	s_mov_b32 m0, s22
	s_nop 0
	global_load_lds_dwordx4 v172, s[0:1]
	s_mov_b32 m0, s24
	s_addc_u32 s3, s3, 0
	s_add_i32 s23, s36, s64
	s_nop 4
	s_mov_b32 s0, m0
	s_mov_b32 m0, s23
	s_nop 0
	global_load_lds_dwordx4 v173, s[2:3]
	s_mov_b32 m0, s0
	global_load_dwordx2 v[166:167], v[146:147], off offset:-8 sc1

; #define LDS_WAIT() asm volatile("s_waitcnt lgkmcnt(0)" ::: "memory")
; __device__ __forceinline__ int crow(int r, int hi) { return (r & 3) + 8 * (r >> 2) + 4 * hi; }
; __device__ __forceinline__ void dsa_step(f32x16& c0, f32x16& c1, f32x16& n0, f32x16& n1, const bool have_n, const LAS char* kpn, const LAS char* vpc, const bf16x8 (&qr)[4], unsigned long long mwn, ...
;     ...
;     f32x2 ps2 = {0.f, 0.f};
; #pragma unroll
;     for (int r = 0; r < 16; r += 2) { c0[r] = __builtin_amdgcn_exp2f(c0[r]); c0[r + 1] = __builtin_amdgcn_exp2f(c0[r + 1]); c1[r] = __builtin_amdgcn_exp2f(c1[r]); c1[r + 1] = __builtin_amdgcn_exp2f(c1[r + 1]);
;         ps2 += (f32x2){c0[r], c0[r + 1]}; ps2 += (f32x2){c1[r], c1[r + 1]}; }
;     lsum += ps2[0] + ps2[1];
;     if (resc) { LDS_WAIT();
; #pragma unroll
;         for (int r = 0; r < 16; ++r) { const float f = wsf[crow(r, hi)]; o[0][r] *= f; o[1][r] *= f; } }
;     pv_mma(o, vf, c0, c1);
;     asm volatile("s_waitcnt vmcnt(0) lgkmcnt(0)\n\ts_barrier" ::: "memory");
; __device__ __forceinline__ void dsa_block_unit(int b, int g, int m  , const bf16_t* Q, const bf16_t* K, const bf16_t* V, const unsigned long long* mask, bf16_t* O, LAS char* L, int wid, int lane, float sbound  ) {
;     ...
;         if (j == jd) break;
;         { const int t_ = sc; sc = sn; sn = sn2; sn2 = t_; } mwn = mwn2;
;         if (j + 3 <= jd) { glds16_s(Kw + (size_t)(j + 3) * 64 * 128, kvoff, kdst + sn2); glds16_s(Vw + (size_t)(j + 3) * 64 * 128, vvoff, vdst + sn2); mwn2 = mrow[j + 3]; }
;         dsa_step(pb0, pb1, pa0, pa1, j + 1 < jd, kp0 + sn, vp0 + sc, qr, mwn, o, mref, lsum, wsf, r32, hi, fixed, tblp);
.LBB0_1767:
	s_or_b64 exec, exec, s[22:23]
	v_exp_f32_e32 v34, v34
	v_exp_f32_e32 v35, v35
	v_exp_f32_e32 v36, v36
	v_exp_f32_e32 v37, v37
	v_exp_f32_e32 v38, v38
	v_exp_f32_e32 v39, v39
	v_exp_f32_e32 v40, v40
	v_exp_f32_e32 v41, v41
	v_cvt_pk_bf16_f32 v186, v34, v35
	v_cvt_pk_bf16_f32 v187, v36, v37
	v_cvt_pk_bf16_f32 v188, v38, v39
	v_cvt_pk_bf16_f32 v189, v40, v41
	v_exp_f32_e32 v42, v42
	v_exp_f32_e32 v43, v43
	v_exp_f32_e32 v44, v44
	v_exp_f32_e32 v45, v45
	v_exp_f32_e32 v46, v46
	v_exp_f32_e32 v47, v47
	v_exp_f32_e32 v48, v48
	v_exp_f32_e32 v49, v49
	s_waitcnt lgkmcnt(14)
	v_mfma_f32_32x32x16_bf16 v[18:33], v[186:189], v[142:145], v[18:33]
	v_exp_f32_e32 v50, v50
	v_exp_f32_e32 v51, v51
	v_cvt_pk_bf16_f32 v142, v42, v43
	v_cvt_pk_bf16_f32 v143, v44, v45
	v_cvt_pk_bf16_f32 v144, v46, v47
	v_cvt_pk_bf16_f32 v145, v48, v49
	v_exp_f32_e32 v52, v52
	s_waitcnt lgkmcnt(10)
	v_mfma_f32_32x32x16_bf16 v[2:17], v[186:189], v[138:141], v[2:17]
	v_exp_f32_e32 v53, v53
	v_pk_add_f32 v[148:149], v[34:35], 0 op_sel_hi:[1,0]
	v_exp_f32_e32 v54, v54
	v_pk_add_f32 v[148:149], v[50:51], v[148:149]
	v_exp_f32_e32 v55, v55
	v_exp_f32_e32 v56, v56
	v_exp_f32_e32 v57, v57
	v_mfma_f32_32x32x16_bf16 v[18:33], v[142:145], v[134:137], v[18:33]
	v_add_f32_e64 v134, v148, v36
	v_add_f32_e64 v135, v149, v37
	v_cvt_pk_bf16_f32 v136, v54, v55
	v_add_f32_e64 v134, v52, v134
	v_add_f32_e64 v135, v53, v135
	v_cvt_pk_bf16_f32 v137, v56, v57
	v_pk_add_f32 v[134:135], v[134:135], v[38:39]
	v_exp_f32_e32 v58, v58
	v_pk_add_f32 v[138:139], v[54:55], v[134:135]
	s_waitcnt lgkmcnt(8)
	v_mfma_f32_32x32x16_bf16 v[2:17], v[142:145], v[130:133], v[2:17]
	v_cvt_pk_bf16_f32 v134, v50, v51
	v_cvt_pk_bf16_f32 v135, v52, v53
	v_exp_f32_e32 v59, v59
	v_exp_f32_e32 v60, v60
	v_exp_f32_e32 v61, v61
	v_exp_f32_e32 v62, v62
	v_exp_f32_e32 v63, v63
	v_exp_f32_e32 v64, v64
	v_exp_f32_e32 v65, v65
	s_waitcnt lgkmcnt(6)
	v_mfma_f32_32x32x16_bf16 v[18:33], v[134:137], v[126:129], v[18:33]
	v_cvt_pk_bf16_f32 v126, v58, v59
	v_cvt_pk_bf16_f32 v127, v60, v61
	v_cvt_pk_bf16_f32 v128, v62, v63
	v_cvt_pk_bf16_f32 v129, v64, v65
	v_add_f32_e64 v130, v138, v40
	v_add_f32_e64 v131, v139, v41
	s_waitcnt vmcnt(0) lgkmcnt(0)
	s_barrier
	s_add_i32 s0, s30, s35
	s_waitcnt lgkmcnt(2)
	v_mfma_f32_32x32x16_bf16 v[2:17], v[134:137], v[122:125], v[2:17]
	v_add_f32_e64 v130, v56, v130
	v_add_f32_e64 v131, v57, v131
	s_cmp_eq_u32 s0, 3
	v_add_f32_e64 v122, v130, v42
	v_add_f32_e64 v123, v131, v43
	v_readfirstlane_b32 s25, v1
	v_pk_add_f32 v[122:123], v[58:59], v[122:123]
	s_nop 0
	v_pk_add_f32 v[122:123], v[122:123], v[44:45]
	v_mfma_f32_32x32x16_bf16 v[18:33], v[126:129], v[118:121], v[18:33]
	v_add_f32_e64 v122, v60, v122
	v_add_f32_e64 v123, v61, v123
	v_add_f32_e64 v118, v122, v46
	v_add_f32_e64 v119, v123, v47
	v_add_f32_e64 v118, v62, v118
	v_add_f32_e64 v119, v63, v119
	v_pk_add_f32 v[118:119], v[118:119], v[48:49]
	s_waitcnt lgkmcnt(0)
	v_mfma_f32_32x32x16_bf16 v[2:17], v[126:129], v[114:117], v[2:17]
	v_add_f32_e64 v118, v64, v118
	v_add_f32_e64 v119, v65, v119
	v_add_f32_e32 v0, v118, v119
	v_add_f32_e32 v157, v157, v0
	v_readfirstlane_b32 s24, v0
	s_cbranch_scc1 .LBB0_1753
	s_cmp_gt_u32 s35, s53
	s_waitcnt vmcnt(0)
	v_mov_b64_e32 v[148:149], v[166:167]
	s_cbranch_scc1 .LBB0_1770
	s_add_u32 s0, s16, s20
	s_addc_u32 s1, s17, s21
	s_add_u32 s0, s0, 0xc000
	s_addc_u32 s1, s1, 0
	s_add_i32 s22, s31, s63
	s_add_u32 s2, s18, s20
	s_addc_u32 s3, s19, s21
	s_add_u32 s2, s2, 0xc000
	s_nop 4
	s_mov_b32 s24, m0
	s_mov_b32 m0, s22
	s_nop 0
	global_load_lds_dwordx4 v172, s[0:1]
	s_mov_b32 m0, s24
	s_addc_u32 s3, s3, 0
	s_add_i32 s23, s31, s64
	s_nop 4
	s_mov_b32 s0, m0
	s_mov_b32 m0, s23
	s_nop 0
	global_load_lds_dwordx4 v173, s[2:3]
	s_mov_b32 m0, s0
	global_load_dwordx2 v[148:149], v[146:147], off sc1

; __device__ __forceinline__ float shfl_xor_f(float v, int mask, int lane) { return __int_as_float(__builtin_amdgcn_ds_bpermute((lane ^ mask) << 2, __float_as_int(v))); }
; __device__ __forceinline__ void quant_rows(unsigned char* ws, size_t xq_off, size_t sar_off, int gw, int NGW, int lane) {
;     const bf16_t* xb = (const bf16_t*)(ws + WS_XB); signed char* xq = (signed char*)(ws + xq_off); float* sar = (float*)(ws + sar_off); const float* ssp = (const float*)(ws + WS_SSP);
;     for (int m = gw; m < M; m += 8 * NGW) {
;         u32x4 a[8][2]; float mx[8];
; #pragma unroll
;         for (int q = 0; q < 8; ++q) { const u32x4* p = (const u32x4*)(xb + (size_t)(m + q * NGW) * D + 16 * lane); a[q][0] = p[0]; a[q][1] = p[1]; }
;         float ssv = 0.f;
;         if (lane < 32) { const f32x4 s4 = *(const f32x4*)(ssp + (size_t)(m + (lane >> 2) * NGW) * 16 + 4 * (lane & 3)); ssv = (s4[0] + s4[1]) + (s4[2] + s4[3]); }
;         ssv += shfl_xor_f(ssv, 1, lane); ssv += shfl_xor_f(ssv, 2, lane);
.LBB0_2005:
	s_ashr_i32 s27, s26, 31
	s_add_i32 s44, s26, s1
	s_lshl_b64 s[24:25], s[26:27], 11
	s_ashr_i32 s45, s44, 31
	s_add_i32 s30, s2, s26
	s_mul_i32 s0, s52, 24
	v_lshl_add_u64 v[2:3], v[66:67], 0, s[24:25]
	s_lshl_b64 s[24:25], s[44:45], 11
	s_ashr_i32 s31, s30, 31
	s_add_i32 s34, s0, s26
	global_load_dwordx4 v[58:61], v[2:3], off offset:16 sc1
	global_load_dwordx4 v[62:65], v[2:3], off sc1
	v_lshl_add_u64 v[2:3], v[66:67], 0, s[24:25]
	s_lshl_b64 s[24:25], s[30:31], 11
	s_ashr_i32 s35, s34, 31
	s_add_i32 s36, s3, s26
	s_mul_i32 s0, s52, 40
	global_load_dwordx4 v[50:53], v[2:3], off offset:16 sc1
	global_load_dwordx4 v[54:57], v[2:3], off sc1
	v_lshl_add_u64 v[2:3], v[66:67], 0, s[24:25]
	s_lshl_b64 s[24:25], s[34:35], 11
	s_ashr_i32 s37, s36, 31
	s_add_i32 s38, s0, s26
	s_mul_i32 s0, s52, 48
	global_load_dwordx4 v[42:45], v[2:3], off offset:16 sc1
	global_load_dwordx4 v[46:49], v[2:3], off sc1
	v_lshl_add_u64 v[2:3], v[66:67], 0, s[24:25]
	s_lshl_b64 s[24:25], s[36:37], 11
	s_ashr_i32 s39, s38, 31
	s_add_i32 s46, s0, s26
	s_mul_i32 s0, s52, 56
	global_load_dwordx4 v[34:37], v[2:3], off offset:16 sc1
	global_load_dwordx4 v[38:41], v[2:3], off sc1
	v_lshl_add_u64 v[2:3], v[66:67], 0, s[24:25]
	s_lshl_b64 s[24:25], s[38:39], 11
	s_ashr_i32 s47, s46, 31
	s_add_i32 s40, s0, s26
	global_load_dwordx4 v[26:29], v[2:3], off offset:16 sc1
	global_load_dwordx4 v[30:33], v[2:3], off sc1
	v_lshl_add_u64 v[2:3], v[66:67], 0, s[24:25]
	s_lshl_b64 s[24:25], s[46:47], 11
	s_ashr_i32 s41, s40, 31
	global_load_dwordx4 v[18:21], v[2:3], off offset:16 sc1
	global_load_dwordx4 v[22:25], v[2:3], off sc1
	v_lshl_add_u64 v[2:3], v[66:67], 0, s[24:25]
	s_lshl_b64 s[24:25], s[40:41], 11
	v_lshl_add_u64 v[6:7], v[66:67], 0, s[24:25]
	global_load_dwordx4 v[10:13], v[2:3], off offset:16 sc1
	global_load_dwordx4 v[14:17], v[2:3], off sc1
	s_nop 0
	global_load_dwordx4 v[2:5], v[6:7], off offset:16 sc1
	s_nop 0
	global_load_dwordx4 v[6:9], v[6:7], off sc1
	s_waitcnt lgkmcnt(0)
	v_mov_b32_e32 v73, 0
	v_add_u32_e32 v72, s26, v74
	s_and_saveexec_b64 s[24:25], s[4:5]
	s_cbranch_execz .LBB0_2007
	v_ashrrev_i32_e32 v73, 31, v72
	v_lshlrev_b64 v[80:81], 6, v[72:73]
	v_lshl_add_u64 v[80:81], v[68:69], 0, v[80:81]
	global_load_dwordx4 v[80:83], v[80:81], off sc1
	s_waitcnt vmcnt(0)
	v_mov_b32_e32 v84, v81
	v_mov_b32_e32 v85, v82
	v_mov_b32_e32 v81, v83
	v_pk_add_f32 v[80:81], v[84:85], v[80:81]
	s_nop 0
	v_add_f32_e32 v73, v80, v81

; __device__ __forceinline__ unsigned xb_add(unsigned* p, unsigned v) { return __hip_atomic_fetch_add(p, v, __ATOMIC_RELAXED, __HIP_MEMORY_SCOPE_AGENT); }
; __device__ __forceinline__ void xcd_barrier_impl(const XcdBarrier& b, bool leader) {
;     ...
;         if (old + 1u == (gen + 1u) * nloc) {
;             __builtin_amdgcn_fence(__ATOMIC_RELEASE, "agent");
;             asm volatile("s_waitcnt vmcnt(0)" ::: "memory");
;             const unsigned og = xb_add(&bar[XB_TOP], 1u);
.LBB0_2146:
	s_andn2_saveexec_b64 s[0:1], s[10:11]
	s_cbranch_execz .LBB0_2163
	s_mov_b64 s[12:13], exec
	s_waitcnt lgkmcnt(0)
	s_waitcnt vmcnt(0)
	v_mbcnt_lo_u32_b32 v2, s12, 0
	s_add_u32 s10, s8, 0x7400
	v_mbcnt_hi_u32_b32 v2, s13, v2
	s_addc_u32 s11, s9, 0
	v_cmp_eq_u32_e32 vcc, 0, v2
	s_and_saveexec_b64 s[14:15], vcc
	s_cbranch_execz .LBB0_2149
	s_bcnt1_i32_b64 s0, s[12:13]
	v_mov_b32_e32 v3, s0
	global_atomic_add v3, v1, v3, s[10:11] sc0
